# hoisted LDS fragment reads in SSD scan stages, LN1 residual loads issued before one wait, barrier leader releases XCD before own invalidate
# speedup vs baseline: 1.0087x; 1.0087x over previous
; __device__ __forceinline__ unsigned xb_add(unsigned* p, unsigned v) { return __hip_atomic_fetch_add(p, v, __ATOMIC_RELAXED, __HIP_MEMORY_SCOPE_AGENT); }
; __device__ __forceinline__ void xcd_barrier(const XcdBarrier& b) {
;     ...
;             __builtin_amdgcn_fence(__ATOMIC_ACQUIRE, "agent");
;             xb_add(&bar[XB_XGEN(b.x)], 1u);
;             asm volatile("s_waitcnt vmcnt(0)" ::: "memory");
.LBB0_234:
	s_or_b64 exec, exec, s[4:5]
	s_mov_b64 s[4:5], exec
	v_mbcnt_lo_u32_b32 v1, s4, 0
	v_mbcnt_hi_u32_b32 v1, s5, v1
	v_cmp_eq_u32_e32 vcc, 0, v1
	s_and_saveexec_b64 s[6:7], vcc
	s_cbranch_execz .LBB0_236
	s_bcnt1_i32_b64 s4, s[4:5]
	v_mov_b32_e32 v1, s4
	v_readlane_b32 s4, v253, 17
	v_readlane_b32 s5, v253, 18
	s_nop 4
	global_atomic_add v3, v1, s[4:5]
.LBB0_236:
	s_or_b64 exec, exec, s[6:7]
	s_waitcnt vmcnt(0)
	buffer_inv sc1
	s_waitcnt vmcnt(0)
.LBB0_237:
	s_or_b64 exec, exec, s[2:3]
	s_waitcnt lgkmcnt(0)
	s_barrier

; __device__ __forceinline__ unsigned xb_add(unsigned* p, unsigned v) { return __hip_atomic_fetch_add(p, v, __ATOMIC_RELAXED, __HIP_MEMORY_SCOPE_AGENT); }
; __device__ __forceinline__ void xcd_barrier(const XcdBarrier& b) {
;     ...
;             __builtin_amdgcn_fence(__ATOMIC_ACQUIRE, "agent");
;             xb_add(&bar[XB_XGEN(b.x)], 1u);
;             asm volatile("s_waitcnt vmcnt(0)" ::: "memory");
; __device__ __forceinline__ void lora_phase(LAS unsigned char* lds, const bf16_t* projb, const float* mix, const float* vmix, const bf16_t* Wl_w, const bf16_t* Wl_a, const bf16_t* Wl_g, const bf16_t* Wl_v, ...
;     ...
;     for (int u = vcu; u < M / 64; u += G) {
;         {
;             const int tau = tid >> 3, part = tid & 7, m = u * 64 + tau; const bool first = (m % SEQ) == 0;
; #pragma unroll
;             for (int i = 0; i < 5; ++i) {
;                 const int j0 = 40 * part + 8 * i;
;                 const u32x4 cur = *(const u32x4*)(projb + (size_t)m * PROJ_BLD + OFF_WLO + j0);
;                 u32x4 prv = (u32x4){0u, 0u, 0u, 0u};
;                 if (!first) prv = *(const u32x4*)(projb + (size_t)(m - 1) * PROJ_BLD + OFF_WLO + j0);
;                 f32x4 mx0, mx1;
;                 if (j0 < 288) { mx0 = *(const f32x4*)(mix + (OFF_WLO - OFF_RW) + j0); mx1 = *(const f32x4*)(mix + (OFF_WLO - OFF_RW) + j0 + 4); }
;                 else if (has_v) { mx0 = *(const f32x4*)(vmix + (j0 - 288)); mx1 = *(const f32x4*)(vmix + (j0 - 288) + 4); }
.LBB0_303:
	s_or_b64 exec, exec, s[4:5]
	s_mov_b64 s[4:5], exec
	v_mbcnt_lo_u32_b32 v1, s4, 0
	v_mbcnt_hi_u32_b32 v1, s5, v1
	v_cmp_eq_u32_e32 vcc, 0, v1
	s_and_saveexec_b64 s[6:7], vcc
	s_cbranch_execz .LBB0_305
	s_bcnt1_i32_b64 s4, s[4:5]
	v_mov_b32_e32 v1, s4
	global_atomic_add v3, v1, s[20:21]
.LBB0_305:
	s_or_b64 exec, exec, s[6:7]
	s_waitcnt vmcnt(0)
	buffer_inv sc1
	s_waitcnt vmcnt(0)
.LBB0_306:
	s_or_b64 exec, exec, s[2:3]
	s_mov_b32 s38, s93
	s_waitcnt lgkmcnt(0)
	s_barrier
	s_ashr_i32 s39, s38, 31
	v_readlane_b32 s2, v253, 4
	v_readlane_b32 s3, v253, 5
	s_add_u32 s36, s2, s38
	v_readlane_b32 s2, v253, 2
	s_addc_u32 s37, s3, s39
	s_add_i32 s60, s38, s2
	v_readlane_b32 s2, v253, 3
	s_add_i32 s61, s38, s2
	s_add_u32 s24, s36, 0x16400000
	s_addc_u32 s25, s37, 0
	s_lshl_b64 s[2:3], s[38:39], 3
	v_readlane_b32 s4, v254, 3
	v_readlane_b32 s5, v254, 4
	s_add_u32 s42, s4, s2
	v_mov_b32_e32 v137, v0
	s_addc_u32 s43, s5, s3
	s_load_dwordx2 s[30:31], s[42:43], 0x48
	s_add_u32 s28, s36, 0x22400000
	s_addc_u32 s29, s37, 0
	v_sub_u32_e64 v1, s14, 1 clamp
	s_cmpk_lt_i32 s61, 0x100
	s_mul_hi_u32 s41, s14, 0xd20
	s_mul_i32 s40, s14, 0xd20
	v_readfirstlane_b32 s39, v1
	v_readfirstlane_b32 s4, v137
	s_cselect_b64 s[2:3], -1, 0
	s_cmpk_gt_i32 s61, 0xff
	v_and_b32_e32 v136, 15, v137
	s_cbranch_scc1 .LBB0_378
	s_load_dwordx2 s[6:7], s[42:43], 0x50
	s_cmp_lg_u32 s14, 0
	s_cselect_b64 s[44:45], -1, 0
	s_lshl_b32 s92, s39, 5
	s_lshl_b64 s[8:9], s[92:93], 2
	s_waitcnt lgkmcnt(0)
	s_add_u32 s10, s6, s8
	s_addc_u32 s11, s7, s9
	s_lshl_b64 s[6:7], s[40:41], 2
	s_add_u32 s6, s30, s6
	v_and_b32_e32 v11, 7, v137
	s_addc_u32 s7, s31, s7
	v_mul_u32_u24_e32 v138, 40, v11
	s_lshl_b32 s4, s4, 1
	s_and_b32 s20, s4, 0xffffff80
	v_lshlrev_b32_e32 v6, 2, v138
	v_mov_b32_e32 v7, v3
	v_ashrrev_i32_e32 v1, 3, v137
	s_movk_i32 s5, 0x290
	s_ashr_i32 s21, s20, 31
	v_lshl_add_u64 v[8:9], s[6:7], 0, v[6:7]
	v_lshl_add_u64 v[144:145], s[10:11], 0, v[6:7]
	v_mov_b32_e32 v7, 0xffffff90
	v_mul_lo_u32 v2, v1, s5
	s_lshl_b64 s[4:5], s[20:21], 1
	v_mad_u32_u24 v7, v11, 40, v7
	v_lshlrev_b32_e32 v4, 1, v136
	s_add_u32 s4, s28, s4
	v_cmp_gt_u32_e64 s[12:13], s50, v7
	v_mov_b32_e32 v7, 0xffffff98
	v_and_b32_e32 v12, 24, v4
	v_and_b32_e32 v4, 48, v137
	s_addc_u32 s5, s29, s5
	v_mov_b32_e32 v5, v3
	v_mad_u32_u24 v7, v11, 40, v7
	v_lshl_add_u64 v[140:141], s[4:5], 0, v[4:5]
	s_mov_b64 s[4:5], 0x3000
	v_mov_b32_e32 v6, 0xffffff88
	v_cmp_gt_u32_e64 s[16:17], s50, v7
	v_mov_b32_e32 v7, 0xffffffa0
	v_and_b32_e32 v13, 3, v137
	v_lshl_add_u64 v[142:143], v[8:9], 0, s[4:5]
	v_lshlrev_b32_e32 v8, 1, v138
	v_mad_u32_u24 v6, v11, 40, v6
	v_mad_u32_u24 v7, v11, 40, v7
	v_add3_u32 v139, 0, v2, v8
	v_mad_u32_u24 v2, v11, 40, 8
	v_cmp_gt_u32_e64 s[10:11], s50, v6
	v_mad_u32_u24 v6, v11, 40, 16
	v_mad_u32_u24 v8, v11, 40, 24
	v_mad_u32_u24 v10, v11, 40, 32
	v_cmp_gt_u32_e64 s[18:19], s50, v7
	v_or3_b32 v146, v12, v13, s20
	v_mul_u32_u24_e32 v7, 0x290, v136
	v_cmp_lt_u32_e64 s[4:5], 1, v11
	v_cmp_lt_u32_e64 s[6:7], 3, v11
	v_cmp_ne_u32_e64 s[8:9], 7, v11
	v_cmp_ne_u32_e64 s[14:15], 0, v11
	v_or_b32_e32 v148, 4, v146
	v_or_b32_e32 v150, 32, v146
	v_or_b32_e32 v152, 36, v146
	v_or_b32_e32 v154, 64, v146
	v_or_b32_e32 v156, 0x44, v146
	v_or_b32_e32 v158, 0x60, v146
	v_or_b32_e32 v160, 0x64, v146
	v_lshl_add_u64 v[162:163], s[36:37], 0, v[4:5]
	v_add3_u32 v147, 0, v4, v7
	v_lshlrev_b32_e32 v164, 1, v2
	v_lshlrev_b32_e32 v166, 1, v6
	v_lshlrev_b32_e32 v168, 1, v8
	v_lshlrev_b32_e32 v170, 1, v10
	s_mov_b32 s50, s61

; __device__ __forceinline__ unsigned xb_add(unsigned* p, unsigned v) { return __hip_atomic_fetch_add(p, v, __ATOMIC_RELAXED, __HIP_MEMORY_SCOPE_AGENT); }
; #define TS_BEGIN(k) do { if (TS_ON(k)) ts_t0 = __builtin_amdgcn_s_memrealtime(); } while (0)
; __device__ __forceinline__ void xcd_barrier(const XcdBarrier& b) {
;     ...
;             __builtin_amdgcn_fence(__ATOMIC_ACQUIRE, "agent");
;             xb_add(&bar[XB_XGEN(b.x)], 1u);
;             asm volatile("s_waitcnt vmcnt(0)" ::: "memory");
; __global__ void __launch_bounds__(NWAVES * 64, 2) fwd(Params P) {
;     ...
;         if (IN(pb + 3)) {
;             PH_BEGIN
;             TS_BEGIN(3);
;     ...
;             RW_ARGS(a);
;             const bool ssd_first = ((vcu >> 1) & 1) != 0;
;             if (ssd_first) { int tid4 = tid; asm volatile("" : "+v"(tid4)); ssd_scan_phase(lds, xbcc, dtb, INP(6) + l * SSD_H, INP(7) + l * SSD_H, (bf16_t*)yssd, vcu, G, tid4); }
.LBB0_655:
	s_or_b64 exec, exec, s[4:5]
	s_mov_b64 s[4:5], exec
	v_mbcnt_lo_u32_b32 v1, s4, 0
	v_mbcnt_hi_u32_b32 v1, s5, v1
	v_cmp_eq_u32_e32 vcc, 0, v1
	s_and_saveexec_b64 s[6:7], vcc
	s_cbranch_execz .LBB0_657
	s_bcnt1_i32_b64 s4, s[4:5]
	v_mov_b32_e32 v1, s4
	global_atomic_add v3, v1, s[40:41]
.LBB0_657:
	s_or_b64 exec, exec, s[6:7]
	s_waitcnt vmcnt(0)
	buffer_inv sc1
	s_waitcnt vmcnt(0)
.LBB0_658:
	s_or_b64 exec, exec, s[2:3]
	s_mov_b32 s4, s93
	s_waitcnt lgkmcnt(0)
	s_barrier
	s_ashr_i32 s5, s4, 31
	v_readlane_b32 s2, v253, 4
	v_readlane_b32 s3, v253, 5
	s_add_u32 s15, s2, s4
	v_readlane_b32 s2, v253, 2
	s_addc_u32 s16, s3, s5
	s_add_i32 s2, s4, s2
	v_writelane_b32 v254, s2, 20
	v_readlane_b32 s2, v253, 3
	s_add_i32 s74, s4, s2
	v_writelane_b32 v254, s4, 21
	s_lshl_b64 s[2:3], s[4:5], 3
	s_waitcnt vmcnt(0)
	v_mov_b32_e32 v1, v0
	v_writelane_b32 v254, s5, 22
	s_nop 0
	v_readlane_b32 s4, v254, 3
	v_readlane_b32 s5, v254, 4
	s_add_u32 s8, s4, s2
	s_addc_u32 s9, s5, s3
	s_add_u32 s2, s8, s64
	s_addc_u32 s3, s9, 0
	s_load_dwordx2 s[2:3], s[2:3], 0x0
	s_add_u32 s4, s8, s63
	s_addc_u32 s5, s9, 0
	s_add_u32 s6, s8, s62
	v_writelane_b32 v254, s8, 23
	s_addc_u32 s7, s9, 0
	s_bitcmp0_b32 s74, 1
	v_writelane_b32 v254, s9, 24
	s_waitcnt lgkmcnt(0)
	v_writelane_b32 v254, s2, 25
	s_cselect_b64 s[78:79], -1, 0
	s_and_b64 vcc, exec, s[78:79]
	v_writelane_b32 v254, s3, 26
	s_load_dwordx2 s[2:3], s[4:5], 0x0
	s_waitcnt lgkmcnt(0)
	v_writelane_b32 v254, s2, 27
	s_nop 1
	v_writelane_b32 v254, s3, 28
	s_load_dwordx2 s[2:3], s[6:7], 0x0
	s_waitcnt lgkmcnt(0)
	v_writelane_b32 v254, s2, 29
	s_nop 1
	v_writelane_b32 v254, s3, 30
	s_cbranch_vccnz .LBB0_733
	v_mov_b32_e32 v2, v1
	s_cmpk_gt_i32 s74, 0xff
	v_readfirstlane_b32 s2, v2
	s_cbranch_scc1 .LBB0_733
	s_add_u32 s4, s15, 0x32400000
	s_addc_u32 s5, s16, 0
	v_writelane_b32 v254, s78, 31
	s_add_u32 s6, s15, 0x35400000
	s_addc_u32 s7, s16, 0
	v_writelane_b32 v254, s79, 32
	v_writelane_b32 v254, s6, 33
	v_and_b32_e32 v7, 63, v2
	v_ashrrev_i32_e32 v106, 2, v2
	v_writelane_b32 v254, s7, 34
	v_and_b32_e32 v10, 3, v2
	v_readlane_b32 s6, v254, 23
	v_readlane_b32 s7, v254, 24
	s_load_dwordx4 s[8:11], s[6:7], 0x30
	v_readlane_b32 s6, v254, 9
	v_readlane_b32 s7, v254, 10
	s_lshl_b64 s[6:7], s[6:7], 2
	v_lshlrev_b32_e32 v7, 3, v7
	s_waitcnt lgkmcnt(0)
; #define LAS __attribute__((address_space(3)))
; __device__ __forceinline__ void ssd_scan_phase(LAS unsigned char* lds, const bf16_t* xbcc, const float* dtb, const float* a_log, const float* dskip, bf16_t* yssd, const int vcu, const int G, const int tid) {
;     const int wave = __builtin_amdgcn_readfirstlane(tid >> 6), lane = tid & 63, fr = lane & 15, fq = lane >> 4;
;     const int lt = (wave < 4) ? 2 * wave : 15 - 2 * wave;
;     LAS bf16_t* Cimg = (LAS bf16_t*)(lds + SS_C); LAS bf16_t* Bimg = (LAS bf16_t*)(lds + SS_B); LAS bf16_t* BTimg = (LAS bf16_t*)(lds + SS_BT);
;     LAS bf16_t* xT = (LAS bf16_t*)(lds + SS_XT); LAS bf16_t* xwT = (LAS bf16_t*)(lds + SS_XW); LAS bf16_t* hT = (LAS bf16_t*)(lds + SS_HT);
;     LAS float* acum = (LAS float*)(lds + SS_AC); LAS float* dtv = (LAS float*)(lds + SS_DT);
;     for (int u = vcu; u < BATCH * SSD_H * 2; u += G) {
;         const int b = u >> 5, h = (u >> 1) & 15, phalf = u & 1, g = h >> 3;
;         const float Ah = -expf(a_log[h]) * 1.4426950408889634f;
;         const float dsk = dskip[h];
;         f32x4 hs[2] = {(f32x4){0.f, 0.f, 0.f, 0.f}, (f32x4){0.f, 0.f, 0.f, 0.f}};
;         for (int i = tid; i < 32 * SP / 2; i += 512) ((LAS unsigned*)hT)[i] = 0u;
;         const int row = tid >> 2, part = tid & 3;
;         u32x4 cvn[4], bvn[4], xrn; float dtn = 0.f, dtn1 = 0.f;
	s_add_u32 s8, s8, s6
	s_addc_u32 s9, s9, s7
	v_writelane_b32 v254, s8, 35
	s_add_u32 s6, s10, s6
	s_addc_u32 s7, s11, s7
	v_writelane_b32 v254, s9, 36
	v_writelane_b32 v254, s6, 37
	s_add_u32 s3, s15, 0x35500000
	v_readlane_b32 s11, v253, 52
	v_writelane_b32 v254, s7, 38
	v_writelane_b32 v254, s15, 39
	v_writelane_b32 v254, s3, 40
	v_writelane_b32 v254, s16, 41
	s_addc_u32 s3, s16, 0
	s_ashr_i32 s8, s2, 6
	v_writelane_b32 v254, s3, 42
	s_lshl_b32 s3, s8, 1
	s_sub_i32 s6, 15, s3
	s_cmp_lt_i32 s8, 4
	s_cselect_b32 s24, s3, s6
	s_movk_i32 s3, 0x880
	s_cmp_lt_u32 s2, 64
	v_cmp_gt_i32_e64 s[6:7], s3, v2
	s_cselect_b64 s[2:3], -1, 0
	s_add_i32 s9, 0, 0x20000
	s_movk_i32 s10, 0x110
	v_add_u32_e32 v108, s9, v7
	v_add_u32_e32 v109, s11, v7
	v_mul_lo_u32 v7, v106, s10
	v_lshlrev_b32_e32 v8, 6, v10
	v_and_b32_e32 v5, 15, v2
	v_add3_u32 v110, 0, v7, v8
	v_and_b32_e32 v7, -4, v2
	v_and_b32_e32 v115, 48, v2
	v_bfe_u32 v9, v2, 4, 2
	v_add_u32_e32 v111, s9, v7
	v_add_u32_e32 v118, s9, v115
	v_readlane_b32 s28, v253, 53
	v_lshl_or_b32 v15, s8, 4, v5
	s_add_i32 s9, 0, 0x11000
	s_lshl_b32 s8, s8, 5
	v_mul_u32_u24_e32 v17, 0x2200, v10
	v_lshlrev_b32_e32 v18, 1, v106
	v_add_u32_e32 v112, s11, v7
	v_add_u32_e32 v7, 0x88, v106
	v_lshl_or_b32 v113, s24, 4, v5
	v_lshlrev_b32_e32 v119, 3, v9
	s_add_i32 s8, s28, s8
	v_add3_u32 v122, s9, v17, v18
	v_mul_u32_u24_e32 v17, 0x440, v10
	v_mul_lo_u32 v8, v113, s10
	v_lshl_add_u32 v116, v113, 2, s11
	v_add_u32_e32 v117, s11, v115
	v_readlane_b32 s11, v253, 54
	v_mul_lo_u32 v15, v15, s10
	v_readlane_b32 s10, v253, 55
	v_add_u32_e32 v16, s8, v119
	v_add_lshl_u32 v18, v17, v106, 1
	v_add_lshl_u32 v17, v7, v17, 1
	s_movk_i32 s8, 0x440
	v_writelane_b32 v254, s6, 44
	v_add_u32_e32 v114, 0, v8
	v_lshlrev_b32_e32 v8, 2, v9
	v_add_u32_e32 v124, s11, v17
	v_add_u32_e32 v126, s10, v17
	v_mad_u32_u24 v17, v10, s8, v237
	v_writelane_b32 v254, s7, 45
	v_add_u32_e32 v123, s11, v18
	v_add_u32_e32 v125, s10, v18
	v_add_lshl_u32 v18, v17, v106, 1
	v_add_lshl_u32 v17, v17, v7, 1
	v_cmp_gt_i32_e64 s[30:31], v8, v113
	v_lshlrev_b32_e32 v4, 5, v10
	v_lshlrev_b32_e32 v6, 3, v10
	v_add_u32_e32 v128, s11, v17
	v_add_u32_e32 v130, s10, v17
	v_mad_u32_u24 v17, v10, s8, v238
	v_mad_u32_u24 v10, v10, s8, v239
	v_writelane_b32 v254, s30, 46
	v_add_u32_e32 v127, s11, v18
	v_add_u32_e32 v129, s10, v18
	v_add_lshl_u32 v18, v17, v106, 1
	v_add_lshl_u32 v17, v17, v7, 1
	v_add_lshl_u32 v7, v10, v7, 1
	v_writelane_b32 v254, s31, 47
	v_cmp_lt_i32_e64 s[30:31], v8, v113
	v_add_u32_e32 v136, s11, v7
	v_add_u32_e32 v138, s10, v7
	v_writelane_b32 v254, s30, 48
	v_or_b32_e32 v7, 3, v8
	v_add_u32_e32 v132, s11, v17
	v_writelane_b32 v254, s31, 49
	v_cmp_gt_i32_e64 s[30:31], v7, v113
	v_add_u32_e32 v134, s10, v17
	v_add_lshl_u32 v17, v10, v106, 1
	v_or_b32_e32 v10, 2, v8
	v_writelane_b32 v254, s30, 50
	v_or_b32_e32 v7, 17, v8
	s_cmp_gt_i32 s24, -1
	v_writelane_b32 v254, s31, 51
	v_cmp_gt_i32_e64 s[30:31], v10, v113
	v_or_b32_e32 v10, 16, v8
	v_add3_u32 v121, s9, v15, v115
	v_writelane_b32 v254, s30, 52
	s_cselect_b64 s[8:9], -1, 0
	s_cmp_gt_i32 s24, 0
	v_writelane_b32 v254, s31, 53
	v_cmp_gt_i32_e64 s[30:31], v7, v113
	v_or_b32_e32 v7, 19, v8
	v_add_u32_e32 v13, s11, v115
	v_writelane_b32 v254, s30, 54
	v_lshl_add_u32 v14, v113, 1, s11
	v_add_u32_e32 v15, s10, v115
	v_writelane_b32 v254, s31, 55
	v_cmp_gt_i32_e64 s[30:31], v10, v113
	v_or_b32_e32 v10, 18, v8
	v_add_u32_e32 v131, s11, v18
	v_writelane_b32 v254, s30, 56
	v_add_u32_e32 v133, s10, v18
	v_add_u32_e32 v135, s11, v17
	v_writelane_b32 v254, s31, 57
	v_cmp_gt_i32_e64 s[30:31], v7, v113
	v_or_b32_e32 v7, 33, v8
	v_add_u32_e32 v137, s10, v17
	v_writelane_b32 v254, s30, 58
	s_cselect_b64 s[10:11], -1, 0
	s_cmp_gt_i32 s24, 1
	v_writelane_b32 v254, s31, 59
	v_cmp_gt_i32_e64 s[30:31], v10, v113
	v_or_b32_e32 v10, 32, v8
	s_cselect_b64 s[12:13], -1, 0
	v_writelane_b32 v254, s30, 60
	s_cmp_gt_i32 s24, 2
	s_cselect_b64 s[14:15], -1, 0
	v_writelane_b32 v254, s31, 61
	v_cmp_gt_i32_e64 s[30:31], v7, v113
	v_or_b32_e32 v7, 35, v8
	s_cmp_gt_i32 s24, 3
	v_writelane_b32 v254, s30, 62
	s_cselect_b64 s[16:17], -1, 0
	s_cmp_gt_i32 s24, 4
	v_writelane_b32 v254, s31, 63
	v_cmp_gt_i32_e64 s[30:31], v10, v113
	v_or_b32_e32 v10, 34, v8
	s_cselect_b64 s[18:19], -1, 0
	v_writelane_b32 v255, s30, 0
	s_cmp_gt_i32 s24, 5
	s_cselect_b64 s[20:21], -1, 0
	v_writelane_b32 v255, s31, 1
	v_cmp_gt_i32_e64 s[30:31], v7, v113
	v_or_b32_e32 v7, 49, v8
	s_cmp_gt_i32 s24, 6
	v_writelane_b32 v255, s30, 2
	v_add_u32_e32 v12, s28, v115
	s_cselect_b64 s[22:23], -1, 0
	v_writelane_b32 v255, s31, 3
	v_cmp_gt_i32_e64 s[30:31], v10, v113
	v_or_b32_e32 v10, 48, v8
	s_cmp_gt_i32 s24, -2
	v_writelane_b32 v255, s30, 4
	v_lshl_add_u32 v140, v2, 2, s28
	v_readlane_b32 s28, v254, 20
	v_writelane_b32 v255, s31, 5
	v_cmp_gt_i32_e64 s[30:31], v7, v113
	v_or_b32_e32 v7, 51, v8
	v_cmp_gt_i32_e64 s[38:39], v7, v113
	v_writelane_b32 v255, s30, 6
	v_or_b32_e32 v7, 0x41, v8
	v_cmp_gt_i32_e64 s[42:43], v7, v113
	v_writelane_b32 v255, s31, 7
	v_cmp_gt_i32_e64 s[30:31], v10, v113
	v_or_b32_e32 v10, 50, v8
	v_cmp_gt_i32_e64 s[40:41], v10, v113
	v_or_b32_e32 v10, 64, v8
	v_or_b32_e32 v7, 0x43, v8
	v_cmp_gt_i32_e64 s[44:45], v10, v113
	v_or_b32_e32 v10, 0x42, v8
	v_cmp_gt_i32_e64 s[46:47], v7, v113
	v_or_b32_e32 v7, 0x51, v8
	v_cmp_gt_i32_e64 s[48:49], v10, v113
	v_or_b32_e32 v10, 0x50, v8
	v_cmp_gt_i32_e64 s[50:51], v7, v113
	v_or_b32_e32 v7, 0x53, v8
	v_cmp_gt_i32_e64 s[52:53], v10, v113
	v_or_b32_e32 v10, 0x52, v8
	v_cmp_gt_i32_e64 s[54:55], v7, v113
	v_or_b32_e32 v7, 0x61, v8
	v_cmp_gt_i32_e64 s[56:57], v10, v113
	v_or_b32_e32 v10, 0x60, v8
	v_cmp_gt_i32_e64 s[58:59], v7, v113
	v_or_b32_e32 v7, 0x63, v8
	v_writelane_b32 v255, s30, 8
	v_cmp_gt_i32_e64 s[60:61], v10, v113
	v_or_b32_e32 v10, 0x62, v8
	v_cmp_gt_i32_e64 s[62:63], v7, v113
	v_or_b32_e32 v7, 0x71, v8
	s_cselect_b64 s[24:25], -1, 0
	v_writelane_b32 v255, s31, 9
	v_cmp_gt_i32_e64 s[64:65], v10, v113
	v_or_b32_e32 v10, 0x70, v8
	v_cmp_gt_i32_e64 s[66:67], v7, v113
	v_or_b32_e32 v7, 0x73, v8
	s_lshl_b32 s28, s28, 6
	v_lshlrev_b32_e32 v107, 1, v2
	v_add_u32_e32 v11, 0, v115
	v_mul_u32_u24_e32 v5, 0x110, v5
	s_mov_b32 s33, s74
	v_cmp_gt_i32_e64 s[68:69], v10, v113
	v_or_b32_e32 v10, 0x72, v8
	v_cmp_gt_i32_e64 s[70:71], v7, v113
	v_mul_u32_u24_e32 v7, 0x440, v9
	v_writelane_b32 v255, s28, 10
	v_cmp_gt_i32_e64 s[6:7], 64, v2
	v_add_u32_e32 v120, v114, v119
	v_cmp_gt_i32_e64 s[72:73], v10, v113
	v_add_u32_e32 v139, 0xfffffe00, v2
	s_lshl_b32 s37, s74, 6
	v_add_u32_e32 v141, 0x80, v107
	v_add_u32_e32 v142, 0x80, v106
	v_lshlrev_b32_e32 v2, 1, v4
	v_lshlrev_b32_e32 v96, 1, v6
	v_lshlrev_b32_e32 v98, 1, v8
	v_add_u32_e32 v143, v14, v7
	v_add_u32_e32 v144, v15, v5
	v_add_u32_e32 v145, v16, v5
	v_add_u32_e32 v146, v11, v5
	v_add_u32_e32 v147, v12, v5
	v_add_u32_e32 v148, v13, v5
	v_writelane_b32 v255, s33, 11
	s_branch .LBB0_662

; #define LAS __attribute__((address_space(3)))
; __device__ __forceinline__ unsigned cvt_pk_bf16(float lo, float hi) { const f32x2 v = {lo, hi}; const bf16x2_t b = __builtin_convertvector(v, bf16x2_t); return __builtin_bit_cast(unsigned, b); }
; __device__ __forceinline__ float bf2f(bf16_t b) { return __uint_as_float(((unsigned)b) << 16); }
; __device__ __forceinline__ void ssd_scan_phase(LAS unsigned char* lds, const bf16_t* xbcc, const float* dtb, const float* a_log, const float* dskip, bf16_t* yssd, const int vcu, const int G, const int tid) {
;     ...
;                 const int l = 16 * lt + fr; const float el = __builtin_amdgcn_exp2f(acum[l]);
; #pragma unroll
;                 for (int pt = 0; pt < 2; ++pt) {
;                     f32x4 o;
; #pragma unroll
;                     for (int r = 0; r < 4; ++r) o[r] = yd[pt][r] + el * yo[pt][r] + dsk * bf2f(xT[(16 * pt + 4 * fq + r) * SP + l]);
;                     { u32x2 w2; w2.x = cvt_pk_bf16(o[0], o[1]); w2.y = cvt_pk_bf16(o[2], o[3]); *(u32x2*)(yssd + (size_t)(mrow0 + l) * 1024 + h * 64 + phalf * 32 + 16 * pt + 4 * fq) = w2; }
;                 }
;             }
;             {
;                 const float ea = __builtin_amdgcn_exp2f(atot);
;                 hs[0] = hs[0] * ea; hs[1] = hs[1] * ea;
; #pragma unroll
;                 for (int ks = 0; ks < 4; ++ks) {
;                     const bf16x8 btf = *(const LAS bf16x8*)(BTimg + (16 * wave + fr) * SP + 32 * ks + 8 * fq);
; #pragma unroll
;                     for (int pt = 0; pt < 2; ++pt) { const bf16x8 xwf = *(const LAS bf16x8*)(xwT + (16 * pt + fr) * SP + 32 * ks + 8 * fq);
;                         hs[pt] = __builtin_amdgcn_mfma_f32_16x16x32_bf16(btf, xwf, hs[pt], 0, 0, 0); }
;                 }
;             }
.LBB0_668:
	ds_read_b32 v64, v116
	v_add_u32_e32 v66, s36, v149
	v_ashrrev_i32_e32 v67, 31, v66
	v_lshlrev_b64 v[66:67], 11, v[66:67]
	v_lshl_add_u64 v[66:67], v[104:105], 0, v[66:67]
	s_waitcnt lgkmcnt(0)
	v_exp_f32_e32 v64, v64
	s_addk_i32 s36, 0x80
	s_waitcnt vmcnt(5)
	v_mov_b64_e32 v[82:83], v[18:19]
	v_mov_b64_e32 v[78:79], v[14:15]
	v_pk_fma_f32 v[52:53], v[60:61], v[64:65], v[52:53] op_sel_hi:[1,0,1]
	ds_read_u16 v60, v143
	ds_read_u16 v61, v143 offset:272
	v_pk_fma_f32 v[54:55], v[62:63], v[64:65], v[54:55] op_sel_hi:[1,0,1]
	v_pk_fma_f32 v[48:49], v[56:57], v[64:65], v[48:49] op_sel_hi:[1,0,1]
	v_pk_fma_f32 v[50:51], v[58:59], v[64:65], v[50:51] op_sel_hi:[1,0,1]
	s_waitcnt lgkmcnt(1)
	v_lshlrev_b32_e32 v60, 16, v60
	s_waitcnt lgkmcnt(0)
	v_lshlrev_b32_e32 v61, 16, v61
	v_pk_fma_f32 v[52:53], v[100:101], v[60:61], v[52:53]
	ds_read_u16 v60, v143 offset:544
	ds_read_u16 v61, v143 offset:816
	v_cvt_pk_bf16_f32 v52, v52, v53
	s_waitcnt vmcnt(3)
	v_mov_b64_e32 v[58:59], v[26:27]
	v_mov_b64_e32 v[74:75], v[10:11]
	s_waitcnt lgkmcnt(1)
	v_lshlrev_b32_e32 v60, 16, v60
	s_waitcnt lgkmcnt(0)
	v_lshlrev_b32_e32 v61, 16, v61
	v_pk_fma_f32 v[54:55], v[100:101], v[60:61], v[54:55]
	s_waitcnt vmcnt(2)
	v_mov_b64_e32 v[62:63], v[30:31]
	v_cvt_pk_bf16_f32 v53, v54, v55
	global_store_dwordx2 v[66:67], v[52:53], off
	ds_read_u16 v52, v143 offset:4352
	ds_read_u16 v53, v143 offset:4624
	v_mov_b64_e32 v[70:71], v[6:7]
	s_cmpk_eq_i32 s36, 0x800
	v_mov_b64_e32 v[60:61], v[28:29]
	s_waitcnt lgkmcnt(1)
	v_lshlrev_b32_e32 v52, 16, v52
	s_waitcnt lgkmcnt(0)
	v_lshlrev_b32_e32 v53, 16, v53
	v_pk_fma_f32 v[48:49], v[100:101], v[52:53], v[48:49]
	ds_read_u16 v52, v143 offset:4896
	ds_read_u16 v53, v143 offset:5168
	v_cvt_pk_bf16_f32 v48, v48, v49
	v_mov_b64_e32 v[56:57], v[24:25]
	v_mov_b64_e32 v[80:81], v[16:17]
	s_waitcnt lgkmcnt(1)
	v_lshlrev_b32_e32 v52, 16, v52
	s_waitcnt lgkmcnt(0)
	v_lshlrev_b32_e32 v53, 16, v53
	v_pk_fma_f32 v[50:51], v[100:101], v[52:53], v[50:51]
	v_mov_b64_e32 v[76:77], v[12:13]
	v_cvt_pk_bf16_f32 v49, v50, v51
	global_store_dwordx2 v[66:67], v[48:49], off offset:32
	v_exp_f32_e32 v48, v97
	s_waitcnt vmcnt(3)
	v_mov_b64_e32 v[66:67], v[34:35]
	v_mov_b64_e32 v[64:65], v[32:33]
	v_mov_b64_e32 v[72:73], v[8:9]
	v_pk_mul_f32 v[42:43], v[42:43], v[48:49] op_sel_hi:[1,0]
	v_pk_mul_f32 v[40:41], v[40:41], v[48:49] op_sel_hi:[1,0]
	v_pk_mul_f32 v[46:47], v[46:47], v[48:49] op_sel_hi:[1,0]
	v_pk_mul_f32 v[44:45], v[44:45], v[48:49] op_sel_hi:[1,0]
	ds_read_b128 v[160:163], v121
	ds_read_b128 v[164:167], v144
	ds_read_b128 v[168:171], v144 offset:4352
	ds_read_b128 v[172:175], v121 offset:64
	ds_read_b128 v[176:179], v144 offset:64
	ds_read_b128 v[180:183], v144 offset:4416
	ds_read_b128 v[184:187], v121 offset:128
	ds_read_b128 v[188:191], v144 offset:128
	ds_read_b128 v[192:195], v144 offset:4480
	ds_read_b128 v[196:199], v144 offset:192
	s_waitcnt lgkmcnt(8)
	v_mfma_f32_16x16x32_bf16 v[40:43], v[160:163], v[164:167], v[40:43]
	v_mov_b64_e32 v[68:69], v[4:5]
	s_waitcnt lgkmcnt(7)
	v_mfma_f32_16x16x32_bf16 v[44:47], v[160:163], v[168:171], v[44:47]
	s_waitcnt lgkmcnt(5)
	v_mfma_f32_16x16x32_bf16 v[40:43], v[172:175], v[176:179], v[40:43]
	s_waitcnt lgkmcnt(4)
	v_mfma_f32_16x16x32_bf16 v[44:47], v[172:175], v[180:183], v[44:47]
	s_waitcnt lgkmcnt(2)
	v_mfma_f32_16x16x32_bf16 v[40:43], v[184:187], v[188:191], v[40:43]
	s_waitcnt lgkmcnt(1)
	v_mfma_f32_16x16x32_bf16 v[44:47], v[184:187], v[192:195], v[44:47]
	ds_read_b128 v[48:51], v121 offset:192
	s_waitcnt lgkmcnt(0)
	v_mfma_f32_16x16x32_bf16 v[40:43], v[48:51], v[196:199], v[40:43]
	ds_read_b128 v[52:55], v144 offset:4544
	s_waitcnt lgkmcnt(0)
	s_barrier
	v_mfma_f32_16x16x32_bf16 v[44:47], v[48:51], v[52:55], v[44:47]
	s_nop 3
	v_cvt_pk_bf16_f32 v48, v40, v41
	v_cvt_pk_bf16_f32 v49, v42, v43
	ds_write_b64 v145, v[48:49]
	s_nop 0
	v_cvt_pk_bf16_f32 v48, v44, v45
	v_cvt_pk_bf16_f32 v49, v46, v47
	ds_write_b64 v145, v[48:49] offset:4352
	v_mov_b64_e32 v[54:55], v[22:23]
	s_waitcnt vmcnt(2)
	v_mov_b64_e32 v[50:51], v[38:39]
	v_mov_b64_e32 v[52:53], v[20:21]
	v_mov_b64_e32 v[48:49], v[36:37]
	s_cbranch_scc1 .LBB0_661

; #define LAS __attribute__((address_space(3)))
; __device__ __forceinline__ unsigned cvt_pk_bf16(float lo, float hi) { const f32x2 v = {lo, hi}; const bf16x2_t b = __builtin_convertvector(v, bf16x2_t); return __builtin_bit_cast(unsigned, b); }
; __device__ __forceinline__ void ssd_scan_phase(LAS unsigned char* lds, const bf16_t* xbcc, const float* dtb, const float* a_log, const float* dskip, bf16_t* yssd, const int vcu, const int G, const int tid) {
;     ...
;                 for (int j = 0; j < 4; ++j) { *(LAS u32x4*)(Cimg + row * SP + 32 * part + 8 * j) = cv[j]; *(LAS u32x4*)(Bimg + row * SP + 32 * part + 8 * j) = bv[j]; }
; #pragma unroll
;                 for (int j = 0; j < 4; ++j) { const unsigned wv[4] = {bv[j].x, bv[j].y, bv[j].z, bv[j].w};
; #pragma unroll
;                     for (int e = 0; e < 4; ++e) { const int n = 32 * part + 8 * j + 2 * e; BTimg[n * SP + row] = (bf16_t)(wv[e] & 0xffffu); BTimg[(n + 1) * SP + row] = (bf16_t)(wv[e] >> 16); } }
;             }
;             __syncthreads();
;             const float atot = acum[127];
;             {
;                 const float wgt = dtv[row] * __builtin_amdgcn_exp2f(atot - acum[row]);
;                 const unsigned wv[4] = {xr.x, xr.y, xr.z, xr.w};
; #pragma unroll
;                 for (int e = 0; e < 4; ++e) { const int p = 8 * part + 2 * e; const float x0 = bf_lo(wv[e]), x1 = bf_hi(wv[e]);
;                     xT[p * SP + row] = (bf16_t)(wv[e] & 0xffffu); xT[(p + 1) * SP + row] = (bf16_t)(wv[e] >> 16);
;                     const unsigned pk = cvt_pk_bf16(x0 * wgt, x1 * wgt); xwT[p * SP + row] = (bf16_t)(pk & 0xffffu); xwT[(p + 1) * SP + row] = (bf16_t)(pk >> 16); }
;             }
;             f32x4 gacc[8];
; #pragma unroll
;             for (int st = 0; st < 8; ++st) gacc[st] = (f32x4){0.f, 0.f, 0.f, 0.f};
;             {
;                 bf16x8 cf[4];
; #pragma unroll
;                 for (int ks = 0; ks < 4; ++ks) cf[ks] = *(const LAS bf16x8*)(Cimg + (16 * lt + fr) * SP + 32 * ks + 8 * fq);
; #pragma unroll
;                 for (int st = 0; st < 8; ++st) if (st <= lt) {
; #pragma unroll
;                     for (int ks = 0; ks < 4; ++ks) { const bf16x8 bfg = *(const LAS bf16x8*)(Bimg + (16 * st + fr) * SP + 32 * ks + 8 * fq);
;                         gacc[st] = __builtin_amdgcn_mfma_f32_16x16x32_bf16(bfg, cf[ks], gacc[st], 0, 0, 0); }
;                 }
.LBB0_676:
	v_readlane_b32 s29, v253, 56
	s_waitcnt vmcnt(14)
	ds_write_b128 v110, v[80:83]
	s_waitcnt vmcnt(10)
	ds_write_b128 v110, v[64:67] offset:34816
	ds_write_b128 v110, v[76:79] offset:16
	ds_write_b128 v110, v[60:63] offset:34832
	ds_write_b128 v110, v[72:75] offset:32
	ds_write_b128 v110, v[56:59] offset:34848
	ds_write_b128 v110, v[68:71] offset:48
	ds_write_b128 v110, v[52:55] offset:34864
	ds_write_b16 v122, v64
	ds_write_b16_d16_hi v122, v64 offset:272
	ds_write_b16 v122, v65 offset:544
	ds_write_b16_d16_hi v122, v65 offset:816
	ds_write_b16 v122, v66 offset:1088
	ds_write_b16_d16_hi v122, v66 offset:1360
	ds_write_b16 v122, v67 offset:1632
	ds_write_b16_d16_hi v122, v67 offset:1904
	ds_write_b16 v122, v60 offset:2176
	ds_write_b16_d16_hi v122, v60 offset:2448
	ds_write_b16 v122, v61 offset:2720
	ds_write_b16_d16_hi v122, v61 offset:2992
	ds_write_b16 v122, v62 offset:3264
	ds_write_b16_d16_hi v122, v62 offset:3536
	ds_write_b16 v122, v63 offset:3808
	ds_write_b16_d16_hi v122, v63 offset:4080
	ds_write_b16 v122, v56 offset:4352
	ds_write_b16_d16_hi v122, v56 offset:4624
	ds_write_b16 v122, v57 offset:4896
	ds_write_b16_d16_hi v122, v57 offset:5168
	ds_write_b16 v122, v58 offset:5440
	ds_write_b16_d16_hi v122, v58 offset:5712
	ds_write_b16 v122, v59 offset:5984
	ds_write_b16_d16_hi v122, v59 offset:6256
	ds_write_b16 v122, v52 offset:6528
	ds_write_b16_d16_hi v122, v52 offset:6800
	ds_write_b16 v122, v53 offset:7072
	ds_write_b16_d16_hi v122, v53 offset:7344
	ds_write_b16 v122, v54 offset:7616
	ds_write_b16_d16_hi v122, v54 offset:7888
	ds_write_b16 v122, v55 offset:8160
	ds_write_b16_d16_hi v122, v55 offset:8432
	v_mov_b32_e32 v52, s29
	s_waitcnt lgkmcnt(0)
	s_barrier
	ds_read_b32 v97, v52
	ds_read_b32 v52, v112
	ds_read_b32 v53, v111
	s_waitcnt vmcnt(9)
	v_lshlrev_b32_e32 v54, 16, v48
	v_and_b32_e32 v55, 0xffff0000, v48
	ds_write_b16 v123, v48
	ds_write_b16_d16_hi v124, v48
	s_waitcnt lgkmcnt(3)
	v_sub_f32_e32 v52, v97, v52
	v_exp_f32_e32 v52, v52
	v_mov_b32_e32 v68, 0
	s_andn2_b64 vcc, exec, s[8:9]
	v_mov_b32_e32 v76, 0
	s_waitcnt lgkmcnt(2)
	v_mul_f32_e32 v52, v53, v52
	v_pk_mul_f32 v[54:55], v[52:53], v[54:55] op_sel_hi:[0,1]
	v_cvt_pk_bf16_f32 v48, v54, v55
	ds_write_b16 v125, v48
	ds_write_b16_d16_hi v126, v48
	ds_write_b16 v127, v49
	ds_write_b16_d16_hi v128, v49
	v_lshlrev_b32_e32 v48, 16, v49
	v_and_b32_e32 v49, 0xffff0000, v49
	v_pk_mul_f32 v[48:49], v[52:53], v[48:49] op_sel_hi:[0,1]
	v_cvt_pk_bf16_f32 v48, v48, v49
	ds_write_b16 v129, v48
	ds_write_b16_d16_hi v130, v48
	ds_write_b16 v131, v50
	ds_write_b16_d16_hi v132, v50
	v_lshlrev_b32_e32 v48, 16, v50
	v_and_b32_e32 v49, 0xffff0000, v50
	v_pk_mul_f32 v[48:49], v[52:53], v[48:49] op_sel_hi:[0,1]
	v_cvt_pk_bf16_f32 v48, v48, v49
	ds_write_b16 v133, v48
	ds_write_b16_d16_hi v134, v48
	ds_write_b16 v135, v51
	ds_write_b16_d16_hi v136, v51
	v_lshlrev_b32_e32 v48, 16, v51
	v_and_b32_e32 v49, 0xffff0000, v51
	v_pk_mul_f32 v[48:49], v[52:53], v[48:49] op_sel_hi:[0,1]
	v_cvt_pk_bf16_f32 v48, v48, v49
	ds_write_b16 v137, v48
	ds_write_b16_d16_hi v138, v48
	v_add_u32_e32 v48, v114, v115
	ds_read_b128 v[92:95], v48
	ds_read_b128 v[88:91], v48 offset:64
	ds_read_b128 v[84:87], v48 offset:128
	ds_read_b128 v[80:83], v48 offset:192
	v_cndmask_b32_e64 v48, 0, 1, s[8:9]
	v_cmp_ne_u32_e64 s[74:75], 1, v48
	v_mov_b32_e32 v77, 0
	v_mov_b32_e32 v78, 0
	v_mov_b32_e32 v79, 0
	s_cbranch_vccnz .LBB0_678
	ds_read_b128 v[160:163], v146 offset:34816
	ds_read_b128 v[164:167], v146 offset:34880
	ds_read_b128 v[168:171], v146 offset:34944
	ds_read_b128 v[172:175], v146 offset:35008
	s_waitcnt lgkmcnt(3)
	v_mfma_f32_16x16x32_bf16 v[48:51], v[160:163], v[92:95], 0
	s_waitcnt lgkmcnt(2)
	v_mfma_f32_16x16x32_bf16 v[48:51], v[164:167], v[88:91], v[48:51]
	s_waitcnt lgkmcnt(1)
	v_mfma_f32_16x16x32_bf16 v[48:51], v[168:171], v[84:87], v[48:51]
	s_waitcnt lgkmcnt(0)
	v_mfma_f32_16x16x32_bf16 v[76:79], v[172:175], v[80:83], v[48:51]
.LBB0_678:
	s_nop 4
	v_cndmask_b32_e64 v48, 0, 1, s[10:11]
	v_cmp_ne_u32_e64 s[88:89], 1, v48
	s_andn2_b64 vcc, exec, s[10:11]
	v_mov_b32_e32 v69, 0
	v_mov_b32_e32 v70, 0
	v_mov_b32_e32 v71, 0
	s_cbranch_vccnz .LBB0_680
	ds_read_b128 v[160:163], v146 offset:39168
	ds_read_b128 v[164:167], v146 offset:39232
	ds_read_b128 v[168:171], v146 offset:39296
	ds_read_b128 v[172:175], v146 offset:39360
	s_waitcnt lgkmcnt(3)
	v_mfma_f32_16x16x32_bf16 v[48:51], v[160:163], v[92:95], 0
	s_waitcnt lgkmcnt(2)
	v_mfma_f32_16x16x32_bf16 v[48:51], v[164:167], v[88:91], v[48:51]
	s_waitcnt lgkmcnt(1)
	v_mfma_f32_16x16x32_bf16 v[48:51], v[168:171], v[84:87], v[48:51]
	s_waitcnt lgkmcnt(0)
	v_mfma_f32_16x16x32_bf16 v[68:71], v[172:175], v[80:83], v[48:51]
; #define LAS __attribute__((address_space(3)))
; __device__ __forceinline__ void ssd_scan_phase(LAS unsigned char* lds, const bf16_t* xbcc, const float* dtb, const float* a_log, const float* dskip, bf16_t* yssd, const int vcu, const int G, const int tid) {
;     ...
;                 for (int st = 0; st < 8; ++st) if (st <= lt) {
; #pragma unroll
;                     for (int ks = 0; ks < 4; ++ks) { const bf16x8 bfg = *(const LAS bf16x8*)(Bimg + (16 * st + fr) * SP + 32 * ks + 8 * fq);
;                         gacc[st] = __builtin_amdgcn_mfma_f32_16x16x32_bf16(bfg, cf[ks], gacc[st], 0, 0, 0); }
;                 }
.LBB0_680:
	s_nop 4
	v_cndmask_b32_e64 v48, 0, 1, s[12:13]
	v_mov_b32_e32 v56, 0
	v_cmp_ne_u32_e64 s[76:77], 1, v48
	s_andn2_b64 vcc, exec, s[12:13]
	v_mov_b32_e32 v72, 0
	v_mov_b32_e32 v73, 0
	v_mov_b32_e32 v74, 0
	v_mov_b32_e32 v75, 0
	s_cbranch_vccnz .LBB0_682
	ds_read_b128 v[160:163], v146 offset:43520
	ds_read_b128 v[164:167], v146 offset:43584
	ds_read_b128 v[168:171], v146 offset:43648
	ds_read_b128 v[172:175], v146 offset:43712
	s_waitcnt lgkmcnt(3)
	v_mfma_f32_16x16x32_bf16 v[48:51], v[160:163], v[92:95], 0
	s_waitcnt lgkmcnt(2)
	v_mfma_f32_16x16x32_bf16 v[48:51], v[164:167], v[88:91], v[48:51]
	s_waitcnt lgkmcnt(1)
	v_mfma_f32_16x16x32_bf16 v[48:51], v[168:171], v[84:87], v[48:51]
	s_waitcnt lgkmcnt(0)
	v_mfma_f32_16x16x32_bf16 v[72:75], v[172:175], v[80:83], v[48:51]
.LBB0_682:
	s_nop 4
	v_cndmask_b32_e64 v48, 0, 1, s[14:15]
	v_cmp_ne_u32_e64 s[84:85], 1, v48
	s_andn2_b64 vcc, exec, s[14:15]
	v_mov_b32_e32 v57, 0
	v_mov_b32_e32 v58, 0
	v_mov_b32_e32 v59, 0
	s_cbranch_vccnz .LBB0_684
	ds_read_b128 v[160:163], v146 offset:47872
	ds_read_b128 v[164:167], v146 offset:47936
	ds_read_b128 v[168:171], v146 offset:48000
	ds_read_b128 v[172:175], v146 offset:48064
	s_waitcnt lgkmcnt(3)
	v_mfma_f32_16x16x32_bf16 v[48:51], v[160:163], v[92:95], 0
	s_waitcnt lgkmcnt(2)
	v_mfma_f32_16x16x32_bf16 v[48:51], v[164:167], v[88:91], v[48:51]
	s_waitcnt lgkmcnt(1)
	v_mfma_f32_16x16x32_bf16 v[48:51], v[168:171], v[84:87], v[48:51]
	s_waitcnt lgkmcnt(0)
	v_mfma_f32_16x16x32_bf16 v[56:59], v[172:175], v[80:83], v[48:51]
.LBB0_684:
	s_nop 4
	v_cndmask_b32_e64 v48, 0, 1, s[16:17]
	v_mov_b32_e32 v52, 0
	v_cmp_ne_u32_e64 s[78:79], 1, v48
	s_andn2_b64 vcc, exec, s[16:17]
	v_mov_b32_e32 v64, 0
	v_mov_b32_e32 v65, 0
	v_mov_b32_e32 v66, 0
	v_mov_b32_e32 v67, 0
	s_cbranch_vccnz .LBB0_686
	ds_read_b128 v[160:163], v146 offset:52224
	ds_read_b128 v[164:167], v146 offset:52288
	ds_read_b128 v[168:171], v146 offset:52352
	ds_read_b128 v[172:175], v146 offset:52416
	s_waitcnt lgkmcnt(3)
	v_mfma_f32_16x16x32_bf16 v[48:51], v[160:163], v[92:95], 0
	s_waitcnt lgkmcnt(2)
	v_mfma_f32_16x16x32_bf16 v[48:51], v[164:167], v[88:91], v[48:51]
	s_waitcnt lgkmcnt(1)
	v_mfma_f32_16x16x32_bf16 v[48:51], v[168:171], v[84:87], v[48:51]
	s_waitcnt lgkmcnt(0)
	v_mfma_f32_16x16x32_bf16 v[64:67], v[172:175], v[80:83], v[48:51]
.LBB0_686:
	s_nop 4
	v_cndmask_b32_e64 v48, 0, 1, s[18:19]
	v_cmp_ne_u32_e64 s[82:83], 1, v48
	s_andn2_b64 vcc, exec, s[18:19]
	v_mov_b32_e32 v53, 0
	v_mov_b32_e32 v54, 0
	v_mov_b32_e32 v55, 0
	s_cbranch_vccnz .LBB0_688
	ds_read_b128 v[160:163], v146 offset:56576
	ds_read_b128 v[164:167], v146 offset:56640
	ds_read_b128 v[168:171], v146 offset:56704
	ds_read_b128 v[172:175], v146 offset:56768
	s_waitcnt lgkmcnt(3)
	v_mfma_f32_16x16x32_bf16 v[48:51], v[160:163], v[92:95], 0
	s_waitcnt lgkmcnt(2)
	v_mfma_f32_16x16x32_bf16 v[48:51], v[164:167], v[88:91], v[48:51]
	s_waitcnt lgkmcnt(1)
	v_mfma_f32_16x16x32_bf16 v[48:51], v[168:171], v[84:87], v[48:51]
	s_waitcnt lgkmcnt(0)
	v_mfma_f32_16x16x32_bf16 v[52:55], v[172:175], v[80:83], v[48:51]
.LBB0_688:
	s_nop 4
	v_cndmask_b32_e64 v49, 0, 1, s[20:21]
	v_mov_b32_e32 v48, 0
	v_cmp_ne_u32_e64 s[80:81], 1, v49
	s_andn2_b64 vcc, exec, s[20:21]
	v_mov_b32_e32 v60, 0
	v_mov_b32_e32 v61, 0
	v_mov_b32_e32 v62, 0
	v_mov_b32_e32 v63, 0
	s_cbranch_vccnz .LBB0_690
	ds_read_b128 v[160:163], v146 offset:60928
	ds_read_b128 v[164:167], v146 offset:60992
	ds_read_b128 v[168:171], v146 offset:61056
	ds_read_b128 v[172:175], v146 offset:61120
	s_waitcnt lgkmcnt(3)
	v_mfma_f32_16x16x32_bf16 v[60:63], v[160:163], v[92:95], 0
	s_waitcnt lgkmcnt(2)
	v_mfma_f32_16x16x32_bf16 v[60:63], v[164:167], v[88:91], v[60:63]
	s_waitcnt lgkmcnt(1)
	v_mfma_f32_16x16x32_bf16 v[60:63], v[168:171], v[84:87], v[60:63]
	s_waitcnt lgkmcnt(0)
	v_mfma_f32_16x16x32_bf16 v[60:63], v[172:175], v[80:83], v[60:63]
.LBB0_690:
	v_cndmask_b32_e64 v49, 0, 1, s[22:23]
	v_cmp_ne_u32_e64 s[86:87], 1, v49
	s_andn2_b64 vcc, exec, s[22:23]
	v_mov_b32_e32 v49, 0
	v_mov_b32_e32 v50, 0
	v_mov_b32_e32 v51, 0
	s_cbranch_vccnz .LBB0_692
	ds_read_b128 v[160:163], v146 offset:65280
	ds_read_b128 v[164:167], v146 offset:65344
	ds_read_b128 v[168:171], v146 offset:65408
	ds_read_b128 v[172:175], v146 offset:65472
	s_waitcnt lgkmcnt(3)
	v_mfma_f32_16x16x32_bf16 v[48:51], v[160:163], v[92:95], 0
	s_waitcnt lgkmcnt(2)
	v_mfma_f32_16x16x32_bf16 v[48:51], v[164:167], v[88:91], v[48:51]
	s_waitcnt lgkmcnt(1)
	v_mfma_f32_16x16x32_bf16 v[48:51], v[168:171], v[84:87], v[48:51]
	s_waitcnt lgkmcnt(0)
	v_mfma_f32_16x16x32_bf16 v[48:51], v[172:175], v[80:83], v[48:51]

; #define LAS __attribute__((address_space(3)))
; __device__ __forceinline__ void ssd_scan_phase(LAS unsigned char* lds, const bf16_t* xbcc, const float* dtb, const float* a_log, const float* dskip, bf16_t* yssd, const int vcu, const int G, const int tid) {
;     ...
;             {
;                 const LAS bf16_t* Mimg = Bimg;
;                 f32x4 yd[2] = {(f32x4){0.f, 0.f, 0.f, 0.f}, (f32x4){0.f, 0.f, 0.f, 0.f}}, yo[2] = {(f32x4){0.f, 0.f, 0.f, 0.f}, (f32x4){0.f, 0.f, 0.f, 0.f}};
; #pragma unroll
;                 for (int ks = 0; ks < 4; ++ks) {
;                     const bf16x8 cfr = *(const LAS bf16x8*)(Cimg + (16 * lt + fr) * SP + 32 * ks + 8 * fq);
; #pragma unroll
;                     for (int pt = 0; pt < 2; ++pt) { const bf16x8 hf = *(const LAS bf16x8*)(hT + (16 * pt + fr) * SP + 32 * ks + 8 * fq);
;                         yo[pt] = __builtin_amdgcn_mfma_f32_16x16x32_bf16(hf, cfr, yo[pt], 0, 0, 0); }
;                     if (2 * ks <= lt) {
;                         const bf16x8 mf = *(const LAS bf16x8*)(Mimg + (16 * lt + fr) * SP + 32 * ks + 8 * fq);
; #pragma unroll
;                         for (int pt = 0; pt < 2; ++pt) { const bf16x8 xf_ = *(const LAS bf16x8*)(xT + (16 * pt + fr) * SP + 32 * ks + 8 * fq);
;                             yd[pt] = __builtin_amdgcn_mfma_f32_16x16x32_bf16(xf_, mf, yd[pt], 0, 0, 0); }
;                     }
;                 }
.LBB0_724:
	s_waitcnt lgkmcnt(0)
	s_barrier
	ds_read_b128 v[48:51], v147
	v_add_u32_e32 v68, v120, v119
	ds_read_b128 v[52:55], v147 offset:4352
	ds_read_b128 v[60:63], v68
	s_mov_b32 s92, s93
	s_mov_b32 s94, s93
	s_mov_b32 s95, s93
	s_waitcnt lgkmcnt(0)
	v_mfma_f32_16x16x32_bf16 v[56:59], v[48:51], v[60:63], 0
	v_mov_b64_e32 v[48:49], s[92:93]
	v_mov_b64_e32 v[50:51], s[94:95]
	s_and_b64 vcc, exec, s[74:75]
	v_mfma_f32_16x16x32_bf16 v[60:63], v[52:55], v[60:63], 0
	v_mov_b64_e32 v[52:53], s[92:93]
	v_mov_b64_e32 v[54:55], s[94:95]
	s_cbranch_vccnz .LBB0_726
	ds_read_b128 v[160:163], v148
	ds_read_b128 v[64:67], v68 offset:34816
	ds_read_b128 v[164:167], v148 offset:4352
	s_waitcnt lgkmcnt(1)
	v_mfma_f32_16x16x32_bf16 v[52:55], v[160:163], v[64:67], 0
	s_waitcnt lgkmcnt(0)
	v_mfma_f32_16x16x32_bf16 v[48:51], v[164:167], v[64:67], 0
.LBB0_726:
	ds_read_b128 v[160:163], v147 offset:64
	ds_read_b128 v[70:73], v68 offset:64
	ds_read_b128 v[164:167], v147 offset:4416
	s_and_b64 vcc, exec, s[76:77]
	s_waitcnt lgkmcnt(1)
	v_mfma_f32_16x16x32_bf16 v[56:59], v[160:163], v[70:73], v[56:59]
	s_waitcnt lgkmcnt(0)
	v_mfma_f32_16x16x32_bf16 v[60:63], v[164:167], v[70:73], v[60:63]
	s_cbranch_vccnz .LBB0_728
	ds_read_b128 v[160:163], v148 offset:64
	ds_read_b128 v[70:73], v68 offset:34880
	ds_read_b128 v[164:167], v148 offset:4416
	s_waitcnt lgkmcnt(1)
	v_mfma_f32_16x16x32_bf16 v[52:55], v[160:163], v[70:73], v[52:55]
	s_waitcnt lgkmcnt(0)
	v_mfma_f32_16x16x32_bf16 v[48:51], v[164:167], v[70:73], v[48:51]
.LBB0_728:
	ds_read_b128 v[160:163], v147 offset:128
	ds_read_b128 v[70:73], v68 offset:128
	ds_read_b128 v[164:167], v147 offset:4480
	s_and_b64 vcc, exec, s[78:79]
	s_waitcnt lgkmcnt(1)
	v_mfma_f32_16x16x32_bf16 v[56:59], v[160:163], v[70:73], v[56:59]
	s_waitcnt lgkmcnt(0)
	v_mfma_f32_16x16x32_bf16 v[64:67], v[164:167], v[70:73], v[60:63]
	s_cbranch_vccnz .LBB0_730
	s_nop 1
	ds_read_b128 v[160:163], v148 offset:128
	ds_read_b128 v[70:73], v68 offset:34944
	ds_read_b128 v[164:167], v148 offset:4480
	s_waitcnt lgkmcnt(1)
	v_mfma_f32_16x16x32_bf16 v[52:55], v[160:163], v[70:73], v[52:55]
	s_waitcnt lgkmcnt(0)
	v_mfma_f32_16x16x32_bf16 v[48:51], v[164:167], v[70:73], v[48:51]
.LBB0_730:
	ds_read_b128 v[160:163], v147 offset:192
	ds_read_b128 v[70:73], v68 offset:192
	ds_read_b128 v[164:167], v147 offset:4544
	s_and_b64 vcc, exec, s[80:81]
	s_waitcnt lgkmcnt(1)
	v_mfma_f32_16x16x32_bf16 v[60:63], v[160:163], v[70:73], v[56:59]
	s_nop 2
	s_waitcnt lgkmcnt(0)
	v_mfma_f32_16x16x32_bf16 v[56:59], v[164:167], v[70:73], v[64:67]
	s_cbranch_vccnz .LBB0_668
	s_nop 1
	ds_read_b128 v[64:67], v68 offset:35008
	ds_read_b128 v[160:163], v148 offset:192
	s_waitcnt lgkmcnt(0)
	v_mfma_f32_16x16x32_bf16 v[52:55], v[160:163], v[64:67], v[52:55]
	ds_read_b128 v[68:71], v148 offset:4544
	s_waitcnt lgkmcnt(0)
	v_mfma_f32_16x16x32_bf16 v[48:51], v[68:71], v[64:67], v[48:51]
	s_branch .LBB0_668

; #define LAS __attribute__((address_space(3)))
; __device__ __forceinline__ unsigned cvt_pk_bf16(float lo, float hi) { const f32x2 v = {lo, hi}; const bf16x2_t b = __builtin_convertvector(v, bf16x2_t); return __builtin_bit_cast(unsigned, b); }
; __device__ __forceinline__ float bf2f(bf16_t b) { return __uint_as_float(((unsigned)b) << 16); }
; __device__ __forceinline__ void ssd_scan_phase(LAS unsigned char* lds, const bf16_t* xbcc, const float* dtb, const float* a_log, const float* dskip, bf16_t* yssd, const int vcu, const int G, const int tid) {
;     ...
;                 const int l = 16 * lt + fr; const float el = __builtin_amdgcn_exp2f(acum[l]);
; #pragma unroll
;                 for (int pt = 0; pt < 2; ++pt) {
;                     f32x4 o;
; #pragma unroll
;                     for (int r = 0; r < 4; ++r) o[r] = yd[pt][r] + el * yo[pt][r] + dsk * bf2f(xT[(16 * pt + 4 * fq + r) * SP + l]);
;                     { u32x2 w2; w2.x = cvt_pk_bf16(o[0], o[1]); w2.y = cvt_pk_bf16(o[2], o[3]); *(u32x2*)(yssd + (size_t)(mrow0 + l) * 1024 + h * 64 + phalf * 32 + 16 * pt + 4 * fq) = w2; }
;                 }
;             }
;             {
;                 const float ea = __builtin_amdgcn_exp2f(atot);
;                 hs[0] = hs[0] * ea; hs[1] = hs[1] * ea;
; #pragma unroll
;                 for (int ks = 0; ks < 4; ++ks) {
;                     const bf16x8 btf = *(const LAS bf16x8*)(BTimg + (16 * wave + fr) * SP + 32 * ks + 8 * fq);
; #pragma unroll
;                     for (int pt = 0; pt < 2; ++pt) { const bf16x8 xwf = *(const LAS bf16x8*)(xwT + (16 * pt + fr) * SP + 32 * ks + 8 * fq);
;                         hs[pt] = __builtin_amdgcn_mfma_f32_16x16x32_bf16(btf, xwf, hs[pt], 0, 0, 0); }
;                 }
;             }
.LBB0_934:
	ds_read_b32 v64, v116
	v_add_u32_e32 v66, s33, v148
	v_ashrrev_i32_e32 v67, 31, v66
	v_lshlrev_b64 v[66:67], 11, v[66:67]
	v_lshl_add_u64 v[66:67], v[104:105], 0, v[66:67]
	s_waitcnt lgkmcnt(0)
	v_exp_f32_e32 v64, v64
	s_addk_i32 s33, 0x80
	s_waitcnt vmcnt(5)
	v_mov_b64_e32 v[82:83], v[18:19]
	v_mov_b64_e32 v[78:79], v[14:15]
	v_pk_fma_f32 v[52:53], v[60:61], v[64:65], v[52:53] op_sel_hi:[1,0,1]
	ds_read_u16 v60, v142
	ds_read_u16 v61, v142 offset:272
	v_pk_fma_f32 v[54:55], v[62:63], v[64:65], v[54:55] op_sel_hi:[1,0,1]
	v_pk_fma_f32 v[48:49], v[56:57], v[64:65], v[48:49] op_sel_hi:[1,0,1]
	v_pk_fma_f32 v[50:51], v[58:59], v[64:65], v[50:51] op_sel_hi:[1,0,1]
	s_waitcnt lgkmcnt(1)
	v_lshlrev_b32_e32 v60, 16, v60
	s_waitcnt lgkmcnt(0)
	v_lshlrev_b32_e32 v61, 16, v61
	v_pk_fma_f32 v[52:53], v[100:101], v[60:61], v[52:53]
	ds_read_u16 v60, v142 offset:544
	ds_read_u16 v61, v142 offset:816
	v_cvt_pk_bf16_f32 v52, v52, v53
	s_waitcnt vmcnt(3)
	v_mov_b64_e32 v[58:59], v[26:27]
	v_mov_b64_e32 v[74:75], v[10:11]
	s_waitcnt lgkmcnt(1)
	v_lshlrev_b32_e32 v60, 16, v60
	s_waitcnt lgkmcnt(0)
	v_lshlrev_b32_e32 v61, 16, v61
	v_pk_fma_f32 v[54:55], v[100:101], v[60:61], v[54:55]
	s_waitcnt vmcnt(2)
	v_mov_b64_e32 v[62:63], v[30:31]
	v_cvt_pk_bf16_f32 v53, v54, v55
	global_store_dwordx2 v[66:67], v[52:53], off
	ds_read_u16 v52, v142 offset:4352
	ds_read_u16 v53, v142 offset:4624
	v_mov_b64_e32 v[70:71], v[6:7]
	s_cmpk_eq_i32 s33, 0x800
	v_mov_b64_e32 v[60:61], v[28:29]
	s_waitcnt lgkmcnt(1)
	v_lshlrev_b32_e32 v52, 16, v52
	s_waitcnt lgkmcnt(0)
	v_lshlrev_b32_e32 v53, 16, v53
	v_pk_fma_f32 v[48:49], v[100:101], v[52:53], v[48:49]
	ds_read_u16 v52, v142 offset:4896
	ds_read_u16 v53, v142 offset:5168
	v_cvt_pk_bf16_f32 v48, v48, v49
	v_mov_b64_e32 v[56:57], v[24:25]
	v_mov_b64_e32 v[80:81], v[16:17]
	s_waitcnt lgkmcnt(1)
	v_lshlrev_b32_e32 v52, 16, v52
	s_waitcnt lgkmcnt(0)
	v_lshlrev_b32_e32 v53, 16, v53
	v_pk_fma_f32 v[50:51], v[100:101], v[52:53], v[50:51]
	v_mov_b64_e32 v[76:77], v[12:13]
	v_cvt_pk_bf16_f32 v49, v50, v51
	global_store_dwordx2 v[66:67], v[48:49], off offset:32
	v_exp_f32_e32 v48, v97
	s_waitcnt vmcnt(3)
	v_mov_b64_e32 v[66:67], v[34:35]
	v_mov_b64_e32 v[64:65], v[32:33]
	v_mov_b64_e32 v[72:73], v[8:9]
	v_pk_mul_f32 v[42:43], v[42:43], v[48:49] op_sel_hi:[1,0]
	v_pk_mul_f32 v[40:41], v[40:41], v[48:49] op_sel_hi:[1,0]
	v_pk_mul_f32 v[46:47], v[46:47], v[48:49] op_sel_hi:[1,0]
	v_pk_mul_f32 v[44:45], v[44:45], v[48:49] op_sel_hi:[1,0]
	ds_read_b128 v[160:163], v121
	ds_read_b128 v[164:167], v143
	ds_read_b128 v[168:171], v143 offset:4352
	ds_read_b128 v[172:175], v121 offset:64
	ds_read_b128 v[176:179], v143 offset:64
	ds_read_b128 v[180:183], v143 offset:4416
	ds_read_b128 v[184:187], v121 offset:128
	ds_read_b128 v[188:191], v143 offset:128
	ds_read_b128 v[192:195], v143 offset:4480
	ds_read_b128 v[196:199], v143 offset:192
	s_waitcnt lgkmcnt(8)
	v_mfma_f32_16x16x32_bf16 v[40:43], v[160:163], v[164:167], v[40:43]
	v_mov_b64_e32 v[68:69], v[4:5]
	s_waitcnt lgkmcnt(7)
	v_mfma_f32_16x16x32_bf16 v[44:47], v[160:163], v[168:171], v[44:47]
	s_waitcnt lgkmcnt(5)
	v_mfma_f32_16x16x32_bf16 v[40:43], v[172:175], v[176:179], v[40:43]
	s_waitcnt lgkmcnt(4)
	v_mfma_f32_16x16x32_bf16 v[44:47], v[172:175], v[180:183], v[44:47]
	s_waitcnt lgkmcnt(2)
	v_mfma_f32_16x16x32_bf16 v[40:43], v[184:187], v[188:191], v[40:43]
	s_waitcnt lgkmcnt(1)
	v_mfma_f32_16x16x32_bf16 v[44:47], v[184:187], v[192:195], v[44:47]
	ds_read_b128 v[48:51], v121 offset:192
	s_waitcnt lgkmcnt(0)
	v_mfma_f32_16x16x32_bf16 v[40:43], v[48:51], v[196:199], v[40:43]
	ds_read_b128 v[52:55], v143 offset:4544
	s_waitcnt lgkmcnt(0)
	s_barrier
	v_mfma_f32_16x16x32_bf16 v[44:47], v[48:51], v[52:55], v[44:47]
	s_nop 3
	v_cvt_pk_bf16_f32 v48, v40, v41
	v_cvt_pk_bf16_f32 v49, v42, v43
	ds_write_b64 v144, v[48:49]
	s_nop 0
	v_cvt_pk_bf16_f32 v48, v44, v45
	v_cvt_pk_bf16_f32 v49, v46, v47
	ds_write_b64 v144, v[48:49] offset:4352
	v_mov_b64_e32 v[54:55], v[22:23]
	s_waitcnt vmcnt(2)
	v_mov_b64_e32 v[50:51], v[38:39]
	v_mov_b64_e32 v[52:53], v[20:21]
	v_mov_b64_e32 v[48:49], v[36:37]
	s_cbranch_scc1 .LBB0_927

; #define LAS __attribute__((address_space(3)))
; __device__ __forceinline__ unsigned cvt_pk_bf16(float lo, float hi) { const f32x2 v = {lo, hi}; const bf16x2_t b = __builtin_convertvector(v, bf16x2_t); return __builtin_bit_cast(unsigned, b); }
; __device__ __forceinline__ void ssd_scan_phase(LAS unsigned char* lds, const bf16_t* xbcc, const float* dtb, const float* a_log, const float* dskip, bf16_t* yssd, const int vcu, const int G, const int tid) {
;     ...
;                 for (int j = 0; j < 4; ++j) { *(LAS u32x4*)(Cimg + row * SP + 32 * part + 8 * j) = cv[j]; *(LAS u32x4*)(Bimg + row * SP + 32 * part + 8 * j) = bv[j]; }
; #pragma unroll
;                 for (int j = 0; j < 4; ++j) { const unsigned wv[4] = {bv[j].x, bv[j].y, bv[j].z, bv[j].w};
; #pragma unroll
;                     for (int e = 0; e < 4; ++e) { const int n = 32 * part + 8 * j + 2 * e; BTimg[n * SP + row] = (bf16_t)(wv[e] & 0xffffu); BTimg[(n + 1) * SP + row] = (bf16_t)(wv[e] >> 16); } }
;             }
;             __syncthreads();
;             const float atot = acum[127];
;             {
;                 const float wgt = dtv[row] * __builtin_amdgcn_exp2f(atot - acum[row]);
;                 const unsigned wv[4] = {xr.x, xr.y, xr.z, xr.w};
; #pragma unroll
;                 for (int e = 0; e < 4; ++e) { const int p = 8 * part + 2 * e; const float x0 = bf_lo(wv[e]), x1 = bf_hi(wv[e]);
;                     xT[p * SP + row] = (bf16_t)(wv[e] & 0xffffu); xT[(p + 1) * SP + row] = (bf16_t)(wv[e] >> 16);
;                     const unsigned pk = cvt_pk_bf16(x0 * wgt, x1 * wgt); xwT[p * SP + row] = (bf16_t)(pk & 0xffffu); xwT[(p + 1) * SP + row] = (bf16_t)(pk >> 16); }
;             }
;             f32x4 gacc[8];
; #pragma unroll
;             for (int st = 0; st < 8; ++st) gacc[st] = (f32x4){0.f, 0.f, 0.f, 0.f};
;             {
;                 bf16x8 cf[4];
; #pragma unroll
;                 for (int ks = 0; ks < 4; ++ks) cf[ks] = *(const LAS bf16x8*)(Cimg + (16 * lt + fr) * SP + 32 * ks + 8 * fq);
; #pragma unroll
;                 for (int st = 0; st < 8; ++st) if (st <= lt) {
; #pragma unroll
;                     for (int ks = 0; ks < 4; ++ks) { const bf16x8 bfg = *(const LAS bf16x8*)(Bimg + (16 * st + fr) * SP + 32 * ks + 8 * fq);
;                         gacc[st] = __builtin_amdgcn_mfma_f32_16x16x32_bf16(bfg, cf[ks], gacc[st], 0, 0, 0); }
;                 }
.LBB0_942:
	v_readlane_b32 s29, v253, 56
	s_waitcnt vmcnt(14)
	ds_write_b128 v110, v[80:83]
	s_waitcnt vmcnt(10)
	ds_write_b128 v110, v[64:67] offset:34816
	ds_write_b128 v110, v[76:79] offset:16
	ds_write_b128 v110, v[60:63] offset:34832
	ds_write_b128 v110, v[72:75] offset:32
	ds_write_b128 v110, v[56:59] offset:34848
	ds_write_b128 v110, v[68:71] offset:48
	ds_write_b128 v110, v[52:55] offset:34864
	ds_write_b16 v122, v64
	ds_write_b16_d16_hi v122, v64 offset:272
	ds_write_b16 v122, v65 offset:544
	ds_write_b16_d16_hi v122, v65 offset:816
	ds_write_b16 v122, v66 offset:1088
	ds_write_b16_d16_hi v122, v66 offset:1360
	ds_write_b16 v122, v67 offset:1632
	ds_write_b16_d16_hi v122, v67 offset:1904
	ds_write_b16 v122, v60 offset:2176
	ds_write_b16_d16_hi v122, v60 offset:2448
	ds_write_b16 v122, v61 offset:2720
	ds_write_b16_d16_hi v122, v61 offset:2992
	ds_write_b16 v122, v62 offset:3264
	ds_write_b16_d16_hi v122, v62 offset:3536
	ds_write_b16 v122, v63 offset:3808
	ds_write_b16_d16_hi v122, v63 offset:4080
	ds_write_b16 v122, v56 offset:4352
	ds_write_b16_d16_hi v122, v56 offset:4624
	ds_write_b16 v122, v57 offset:4896
	ds_write_b16_d16_hi v122, v57 offset:5168
	ds_write_b16 v122, v58 offset:5440
	ds_write_b16_d16_hi v122, v58 offset:5712
	ds_write_b16 v122, v59 offset:5984
	ds_write_b16_d16_hi v122, v59 offset:6256
	ds_write_b16 v122, v52 offset:6528
	ds_write_b16_d16_hi v122, v52 offset:6800
	ds_write_b16 v122, v53 offset:7072
	ds_write_b16_d16_hi v122, v53 offset:7344
	ds_write_b16 v122, v54 offset:7616
	ds_write_b16_d16_hi v122, v54 offset:7888
	ds_write_b16 v122, v55 offset:8160
	ds_write_b16_d16_hi v122, v55 offset:8432
	v_mov_b32_e32 v52, s29
	s_waitcnt lgkmcnt(0)
	s_barrier
	ds_read_b32 v97, v52
	ds_read_b32 v52, v112
	ds_read_b32 v53, v111
	s_waitcnt vmcnt(9)
	v_lshlrev_b32_e32 v54, 16, v48
	v_and_b32_e32 v55, 0xffff0000, v48
	ds_write_b16 v123, v48
	ds_write_b16_d16_hi v124, v48
	s_waitcnt lgkmcnt(3)
	v_sub_f32_e32 v52, v97, v52
	v_exp_f32_e32 v52, v52
	v_mov_b32_e32 v64, 0
	s_andn2_b64 vcc, exec, s[8:9]
	v_mov_b32_e32 v76, 0
	s_waitcnt lgkmcnt(2)
	v_mul_f32_e32 v52, v53, v52
	v_pk_mul_f32 v[54:55], v[52:53], v[54:55] op_sel_hi:[0,1]
	v_cvt_pk_bf16_f32 v48, v54, v55
	ds_write_b16 v125, v48
	ds_write_b16_d16_hi v126, v48
	ds_write_b16 v127, v49
	ds_write_b16_d16_hi v128, v49
	v_lshlrev_b32_e32 v48, 16, v49
	v_and_b32_e32 v49, 0xffff0000, v49
	v_pk_mul_f32 v[48:49], v[52:53], v[48:49] op_sel_hi:[0,1]
	v_cvt_pk_bf16_f32 v48, v48, v49
	ds_write_b16 v129, v48
	ds_write_b16_d16_hi v130, v48
	ds_write_b16 v131, v50
	ds_write_b16_d16_hi v132, v50
	v_lshlrev_b32_e32 v48, 16, v50
	v_and_b32_e32 v49, 0xffff0000, v50
	v_pk_mul_f32 v[48:49], v[52:53], v[48:49] op_sel_hi:[0,1]
	v_cvt_pk_bf16_f32 v48, v48, v49
	ds_write_b16 v133, v48
	ds_write_b16_d16_hi v134, v48
	ds_write_b16 v135, v51
	ds_write_b16_d16_hi v136, v51
	v_lshlrev_b32_e32 v48, 16, v51
	v_and_b32_e32 v49, 0xffff0000, v51
	v_pk_mul_f32 v[48:49], v[52:53], v[48:49] op_sel_hi:[0,1]
	v_cvt_pk_bf16_f32 v48, v48, v49
	ds_write_b16 v137, v48
	ds_write_b16_d16_hi v138, v48
	v_add_u32_e32 v48, v114, v115
	ds_read_b128 v[92:95], v48
	ds_read_b128 v[88:91], v48 offset:64
	ds_read_b128 v[84:87], v48 offset:128
	ds_read_b128 v[80:83], v48 offset:192
	v_cndmask_b32_e64 v48, 0, 1, s[8:9]
	v_cmp_ne_u32_e64 s[74:75], 1, v48
	v_mov_b32_e32 v77, 0
	v_mov_b32_e32 v78, 0
	v_mov_b32_e32 v79, 0
	s_cbranch_vccnz .LBB0_944
	ds_read_b128 v[160:163], v145 offset:34816
	ds_read_b128 v[164:167], v145 offset:34880
	ds_read_b128 v[168:171], v145 offset:34944
	ds_read_b128 v[172:175], v145 offset:35008
	s_waitcnt lgkmcnt(3)
	v_mfma_f32_16x16x32_bf16 v[48:51], v[160:163], v[92:95], 0
	s_waitcnt lgkmcnt(2)
	v_mfma_f32_16x16x32_bf16 v[48:51], v[164:167], v[88:91], v[48:51]
	s_waitcnt lgkmcnt(1)
	v_mfma_f32_16x16x32_bf16 v[48:51], v[168:171], v[84:87], v[48:51]
	s_waitcnt lgkmcnt(0)
	v_mfma_f32_16x16x32_bf16 v[76:79], v[172:175], v[80:83], v[48:51]
.LBB0_944:
	s_nop 4
	v_cndmask_b32_e64 v48, 0, 1, s[10:11]
	v_cmp_ne_u32_e64 s[88:89], 1, v48
	s_andn2_b64 vcc, exec, s[10:11]
	v_mov_b32_e32 v65, 0
	v_mov_b32_e32 v66, 0
	v_mov_b32_e32 v67, 0
	s_cbranch_vccnz .LBB0_946
	ds_read_b128 v[160:163], v145 offset:39168
	ds_read_b128 v[164:167], v145 offset:39232
	ds_read_b128 v[168:171], v145 offset:39296
	ds_read_b128 v[172:175], v145 offset:39360
	s_waitcnt lgkmcnt(3)
	v_mfma_f32_16x16x32_bf16 v[48:51], v[160:163], v[92:95], 0
	s_waitcnt lgkmcnt(2)
	v_mfma_f32_16x16x32_bf16 v[48:51], v[164:167], v[88:91], v[48:51]
	s_waitcnt lgkmcnt(1)
	v_mfma_f32_16x16x32_bf16 v[48:51], v[168:171], v[84:87], v[48:51]
	s_waitcnt lgkmcnt(0)
	v_mfma_f32_16x16x32_bf16 v[64:67], v[172:175], v[80:83], v[48:51]
; #define LAS __attribute__((address_space(3)))
; __device__ __forceinline__ void ssd_scan_phase(LAS unsigned char* lds, const bf16_t* xbcc, const float* dtb, const float* a_log, const float* dskip, bf16_t* yssd, const int vcu, const int G, const int tid) {
;     ...
;                 for (int st = 0; st < 8; ++st) if (st <= lt) {
; #pragma unroll
;                     for (int ks = 0; ks < 4; ++ks) { const bf16x8 bfg = *(const LAS bf16x8*)(Bimg + (16 * st + fr) * SP + 32 * ks + 8 * fq);
;                         gacc[st] = __builtin_amdgcn_mfma_f32_16x16x32_bf16(bfg, cf[ks], gacc[st], 0, 0, 0); }
;                 }
.LBB0_946:
	s_nop 4
	v_cndmask_b32_e64 v48, 0, 1, s[12:13]
	v_mov_b32_e32 v56, 0
	v_cmp_ne_u32_e64 s[76:77], 1, v48
	s_andn2_b64 vcc, exec, s[12:13]
	v_mov_b32_e32 v72, 0
	v_mov_b32_e32 v73, 0
	v_mov_b32_e32 v74, 0
	v_mov_b32_e32 v75, 0
	s_cbranch_vccnz .LBB0_948
	ds_read_b128 v[160:163], v145 offset:43520
	ds_read_b128 v[164:167], v145 offset:43584
	ds_read_b128 v[168:171], v145 offset:43648
	ds_read_b128 v[172:175], v145 offset:43712
	s_waitcnt lgkmcnt(3)
	v_mfma_f32_16x16x32_bf16 v[48:51], v[160:163], v[92:95], 0
	s_waitcnt lgkmcnt(2)
	v_mfma_f32_16x16x32_bf16 v[48:51], v[164:167], v[88:91], v[48:51]
	s_waitcnt lgkmcnt(1)
	v_mfma_f32_16x16x32_bf16 v[48:51], v[168:171], v[84:87], v[48:51]
	s_waitcnt lgkmcnt(0)
	v_mfma_f32_16x16x32_bf16 v[72:75], v[172:175], v[80:83], v[48:51]
.LBB0_948:
	s_nop 4
	v_cndmask_b32_e64 v48, 0, 1, s[14:15]
	v_cmp_ne_u32_e64 s[84:85], 1, v48
	s_andn2_b64 vcc, exec, s[14:15]
	v_mov_b32_e32 v57, 0
	v_mov_b32_e32 v58, 0
	v_mov_b32_e32 v59, 0
	s_cbranch_vccnz .LBB0_950
	ds_read_b128 v[160:163], v145 offset:47872
	ds_read_b128 v[164:167], v145 offset:47936
	ds_read_b128 v[168:171], v145 offset:48000
	ds_read_b128 v[172:175], v145 offset:48064
	s_waitcnt lgkmcnt(3)
	v_mfma_f32_16x16x32_bf16 v[48:51], v[160:163], v[92:95], 0
	s_waitcnt lgkmcnt(2)
	v_mfma_f32_16x16x32_bf16 v[48:51], v[164:167], v[88:91], v[48:51]
	s_waitcnt lgkmcnt(1)
	v_mfma_f32_16x16x32_bf16 v[48:51], v[168:171], v[84:87], v[48:51]
	s_waitcnt lgkmcnt(0)
	v_mfma_f32_16x16x32_bf16 v[56:59], v[172:175], v[80:83], v[48:51]
.LBB0_950:
	s_nop 4
	v_cndmask_b32_e64 v48, 0, 1, s[16:17]
	v_mov_b32_e32 v52, 0
	v_cmp_ne_u32_e64 s[78:79], 1, v48
	s_andn2_b64 vcc, exec, s[16:17]
	v_mov_b32_e32 v68, 0
	v_mov_b32_e32 v69, 0
	v_mov_b32_e32 v70, 0
	v_mov_b32_e32 v71, 0
	s_cbranch_vccnz .LBB0_952
	ds_read_b128 v[160:163], v145 offset:52224
	ds_read_b128 v[164:167], v145 offset:52288
	ds_read_b128 v[168:171], v145 offset:52352
	ds_read_b128 v[172:175], v145 offset:52416
	s_waitcnt lgkmcnt(3)
	v_mfma_f32_16x16x32_bf16 v[48:51], v[160:163], v[92:95], 0
	s_waitcnt lgkmcnt(2)
	v_mfma_f32_16x16x32_bf16 v[48:51], v[164:167], v[88:91], v[48:51]
	s_waitcnt lgkmcnt(1)
	v_mfma_f32_16x16x32_bf16 v[48:51], v[168:171], v[84:87], v[48:51]
	s_waitcnt lgkmcnt(0)
	v_mfma_f32_16x16x32_bf16 v[68:71], v[172:175], v[80:83], v[48:51]
.LBB0_952:
	s_nop 4
	v_cndmask_b32_e64 v48, 0, 1, s[18:19]
	v_cmp_ne_u32_e64 s[82:83], 1, v48
	s_andn2_b64 vcc, exec, s[18:19]
	v_mov_b32_e32 v53, 0
	v_mov_b32_e32 v54, 0
	v_mov_b32_e32 v55, 0
	s_cbranch_vccnz .LBB0_954
	ds_read_b128 v[160:163], v145 offset:56576
	ds_read_b128 v[164:167], v145 offset:56640
	ds_read_b128 v[168:171], v145 offset:56704
	ds_read_b128 v[172:175], v145 offset:56768
	s_waitcnt lgkmcnt(3)
	v_mfma_f32_16x16x32_bf16 v[48:51], v[160:163], v[92:95], 0
	s_waitcnt lgkmcnt(2)
	v_mfma_f32_16x16x32_bf16 v[48:51], v[164:167], v[88:91], v[48:51]
	s_waitcnt lgkmcnt(1)
	v_mfma_f32_16x16x32_bf16 v[48:51], v[168:171], v[84:87], v[48:51]
	s_waitcnt lgkmcnt(0)
	v_mfma_f32_16x16x32_bf16 v[52:55], v[172:175], v[80:83], v[48:51]
.LBB0_954:
	s_nop 4
	v_cndmask_b32_e64 v49, 0, 1, s[20:21]
	v_mov_b32_e32 v48, 0
	v_cmp_ne_u32_e64 s[80:81], 1, v49
	s_andn2_b64 vcc, exec, s[20:21]
	v_mov_b32_e32 v60, 0
	v_mov_b32_e32 v61, 0
	v_mov_b32_e32 v62, 0
	v_mov_b32_e32 v63, 0
	s_cbranch_vccnz .LBB0_956
	ds_read_b128 v[160:163], v145 offset:60928
	ds_read_b128 v[164:167], v145 offset:60992
	ds_read_b128 v[168:171], v145 offset:61056
	ds_read_b128 v[172:175], v145 offset:61120
	s_waitcnt lgkmcnt(3)
	v_mfma_f32_16x16x32_bf16 v[60:63], v[160:163], v[92:95], 0
	s_waitcnt lgkmcnt(2)
	v_mfma_f32_16x16x32_bf16 v[60:63], v[164:167], v[88:91], v[60:63]
	s_waitcnt lgkmcnt(1)
	v_mfma_f32_16x16x32_bf16 v[60:63], v[168:171], v[84:87], v[60:63]
	s_waitcnt lgkmcnt(0)
	v_mfma_f32_16x16x32_bf16 v[60:63], v[172:175], v[80:83], v[60:63]
.LBB0_956:
	v_cndmask_b32_e64 v49, 0, 1, s[22:23]
	v_cmp_ne_u32_e64 s[86:87], 1, v49
	s_andn2_b64 vcc, exec, s[22:23]
	v_mov_b32_e32 v49, 0
	v_mov_b32_e32 v50, 0
	v_mov_b32_e32 v51, 0
	s_cbranch_vccnz .LBB0_958
	ds_read_b128 v[160:163], v145 offset:65280
	ds_read_b128 v[164:167], v145 offset:65344
	ds_read_b128 v[168:171], v145 offset:65408
	ds_read_b128 v[172:175], v145 offset:65472
	s_waitcnt lgkmcnt(3)
	v_mfma_f32_16x16x32_bf16 v[48:51], v[160:163], v[92:95], 0
	s_waitcnt lgkmcnt(2)
	v_mfma_f32_16x16x32_bf16 v[48:51], v[164:167], v[88:91], v[48:51]
	s_waitcnt lgkmcnt(1)
	v_mfma_f32_16x16x32_bf16 v[48:51], v[168:171], v[84:87], v[48:51]
	s_waitcnt lgkmcnt(0)
	v_mfma_f32_16x16x32_bf16 v[48:51], v[172:175], v[80:83], v[48:51]

; #define LAS __attribute__((address_space(3)))
; __device__ __forceinline__ void ssd_scan_phase(LAS unsigned char* lds, const bf16_t* xbcc, const float* dtb, const float* a_log, const float* dskip, bf16_t* yssd, const int vcu, const int G, const int tid) {
;     ...
;             {
;                 const LAS bf16_t* Mimg = Bimg;
;                 f32x4 yd[2] = {(f32x4){0.f, 0.f, 0.f, 0.f}, (f32x4){0.f, 0.f, 0.f, 0.f}}, yo[2] = {(f32x4){0.f, 0.f, 0.f, 0.f}, (f32x4){0.f, 0.f, 0.f, 0.f}};
; #pragma unroll
;                 for (int ks = 0; ks < 4; ++ks) {
;                     const bf16x8 cfr = *(const LAS bf16x8*)(Cimg + (16 * lt + fr) * SP + 32 * ks + 8 * fq);
; #pragma unroll
;                     for (int pt = 0; pt < 2; ++pt) { const bf16x8 hf = *(const LAS bf16x8*)(hT + (16 * pt + fr) * SP + 32 * ks + 8 * fq);
;                         yo[pt] = __builtin_amdgcn_mfma_f32_16x16x32_bf16(hf, cfr, yo[pt], 0, 0, 0); }
;                     if (2 * ks <= lt) {
;                         const bf16x8 mf = *(const LAS bf16x8*)(Mimg + (16 * lt + fr) * SP + 32 * ks + 8 * fq);
; #pragma unroll
;                         for (int pt = 0; pt < 2; ++pt) { const bf16x8 xf_ = *(const LAS bf16x8*)(xT + (16 * pt + fr) * SP + 32 * ks + 8 * fq);
;                             yd[pt] = __builtin_amdgcn_mfma_f32_16x16x32_bf16(xf_, mf, yd[pt], 0, 0, 0); }
;                     }
;                 }
.LBB0_990:
	s_waitcnt lgkmcnt(0)
	s_barrier
	ds_read_b128 v[48:51], v146
	v_add_u32_e32 v68, v120, v119
	ds_read_b128 v[52:55], v146 offset:4352
	ds_read_b128 v[60:63], v68
	s_mov_b32 s92, s93
	s_mov_b32 s94, s93
	s_mov_b32 s95, s93
	s_waitcnt lgkmcnt(0)
	v_mfma_f32_16x16x32_bf16 v[56:59], v[48:51], v[60:63], 0
	v_mov_b64_e32 v[48:49], s[92:93]
	v_mov_b64_e32 v[50:51], s[94:95]
	s_and_b64 vcc, exec, s[74:75]
	v_mfma_f32_16x16x32_bf16 v[60:63], v[52:55], v[60:63], 0
	v_mov_b64_e32 v[52:53], s[92:93]
	v_mov_b64_e32 v[54:55], s[94:95]
	s_cbranch_vccnz .LBB0_992
	ds_read_b128 v[160:163], v147
	ds_read_b128 v[64:67], v68 offset:34816
	ds_read_b128 v[164:167], v147 offset:4352
	s_waitcnt lgkmcnt(1)
	v_mfma_f32_16x16x32_bf16 v[52:55], v[160:163], v[64:67], 0
	s_waitcnt lgkmcnt(0)
	v_mfma_f32_16x16x32_bf16 v[48:51], v[164:167], v[64:67], 0
.LBB0_992:
	ds_read_b128 v[160:163], v146 offset:64
	ds_read_b128 v[70:73], v68 offset:64
	ds_read_b128 v[164:167], v146 offset:4416
	s_and_b64 vcc, exec, s[76:77]
	s_waitcnt lgkmcnt(1)
	v_mfma_f32_16x16x32_bf16 v[56:59], v[160:163], v[70:73], v[56:59]
	s_waitcnt lgkmcnt(0)
	v_mfma_f32_16x16x32_bf16 v[60:63], v[164:167], v[70:73], v[60:63]
	s_cbranch_vccnz .LBB0_994
	ds_read_b128 v[160:163], v147 offset:64
	ds_read_b128 v[70:73], v68 offset:34880
	ds_read_b128 v[164:167], v147 offset:4416
	s_waitcnt lgkmcnt(1)
	v_mfma_f32_16x16x32_bf16 v[52:55], v[160:163], v[70:73], v[52:55]
	s_waitcnt lgkmcnt(0)
	v_mfma_f32_16x16x32_bf16 v[48:51], v[164:167], v[70:73], v[48:51]
.LBB0_994:
	ds_read_b128 v[160:163], v146 offset:128
	ds_read_b128 v[70:73], v68 offset:128
	ds_read_b128 v[164:167], v146 offset:4480
	s_and_b64 vcc, exec, s[78:79]
	s_waitcnt lgkmcnt(1)
	v_mfma_f32_16x16x32_bf16 v[56:59], v[160:163], v[70:73], v[56:59]
	s_waitcnt lgkmcnt(0)
	v_mfma_f32_16x16x32_bf16 v[64:67], v[164:167], v[70:73], v[60:63]
	s_cbranch_vccnz .LBB0_996
	s_nop 1
	ds_read_b128 v[160:163], v147 offset:128
	ds_read_b128 v[70:73], v68 offset:34944
	ds_read_b128 v[164:167], v147 offset:4480
	s_waitcnt lgkmcnt(1)
	v_mfma_f32_16x16x32_bf16 v[52:55], v[160:163], v[70:73], v[52:55]
	s_waitcnt lgkmcnt(0)
	v_mfma_f32_16x16x32_bf16 v[48:51], v[164:167], v[70:73], v[48:51]
.LBB0_996:
	ds_read_b128 v[160:163], v146 offset:192
	ds_read_b128 v[70:73], v68 offset:192
	ds_read_b128 v[164:167], v146 offset:4544
	s_and_b64 vcc, exec, s[80:81]
	s_waitcnt lgkmcnt(1)
	v_mfma_f32_16x16x32_bf16 v[60:63], v[160:163], v[70:73], v[56:59]
	s_nop 2
	s_waitcnt lgkmcnt(0)
	v_mfma_f32_16x16x32_bf16 v[56:59], v[164:167], v[70:73], v[64:67]
	s_cbranch_vccnz .LBB0_934
	s_nop 1
	ds_read_b128 v[64:67], v68 offset:35008
	ds_read_b128 v[160:163], v147 offset:192
	ds_read_b128 v[164:167], v147 offset:4544
	s_waitcnt lgkmcnt(1)
	v_mfma_f32_16x16x32_bf16 v[52:55], v[160:163], v[64:67], v[52:55]
	s_waitcnt lgkmcnt(0)
	v_mfma_f32_16x16x32_bf16 v[48:51], v[164:167], v[64:67], v[48:51]
	s_branch .LBB0_934

; __device__ __forceinline__ unsigned xb_add(unsigned* p, unsigned v) { return __hip_atomic_fetch_add(p, v, __ATOMIC_RELAXED, __HIP_MEMORY_SCOPE_AGENT); }
; __device__ __forceinline__ void xcd_barrier(const XcdBarrier& b) {
;     ...
;             __builtin_amdgcn_fence(__ATOMIC_ACQUIRE, "agent");
;             xb_add(&bar[XB_XGEN(b.x)], 1u);
;             asm volatile("s_waitcnt vmcnt(0)" ::: "memory");
; __device__ __forceinline__ void rwkv_post_phase(const bf16_t* __restrict__ yrw, const bf16_t* __restrict__ bon, const bf16_t* __restrict__ lw_g, const float* __restrict__ ln_w, const float* __restrict__ ln_b, bf16_t* __restrict__ ymixb, const int gw, const int NGW, const int lane) {
;     const int c0 = 16 * lane;
;     f32x4 lw4[4], lb4[4];
; #pragma unroll
;     for (int j = 0; j < 4; ++j) { lw4[j] = *(const f32x4*)(ln_w + c0 + 4 * j); lb4[j] = *(const f32x4*)(ln_b + c0 + 4 * j); }
; #pragma unroll 2
;     for (int m = gw; m < M; m += NGW) {
.LBB0_1050:
	s_or_b64 exec, exec, s[6:7]
	s_waitcnt vmcnt(0)
	buffer_inv sc1
	s_waitcnt vmcnt(0)
.LBB0_1051:
	s_or_b64 exec, exec, s[2:3]
	s_mov_b32 s4, s93
	s_waitcnt vmcnt(1)
	v_mov_b32_e32 v36, v0
	v_readlane_b32 s2, v253, 3
	s_waitcnt lgkmcnt(0)
	s_barrier
	s_add_i32 s2, s4, s2
	v_readfirstlane_b32 s3, v36
	s_ashr_i32 s3, s3, 6
	s_lshl_b32 s2, s2, 3
	s_add_i32 s6, s3, s2
	s_cmpk_gt_i32 s6, 0x3fff
	s_mov_b64 s[2:3], -1
	s_cbranch_scc0 .LBB0_1053
	s_mov_b64 s[2:3], 0

;     __device__ void init2(int Mrows, int N, int G_, int c_, int reps_) { init(Mrows, N, G_, c_); per = (nwg + G - 1) / G; reps = reps_; }
; __device__ __forceinline__ unsigned xb_add(unsigned* p, unsigned v) { return __hip_atomic_fetch_add(p, v, __ATOMIC_RELAXED, __HIP_MEMORY_SCOPE_AGENT); }
; #define TS_BEGIN(k) do { if (TS_ON(k)) ts_t0 = __builtin_amdgcn_s_memrealtime(); } while (0)
; __device__ __forceinline__ void xcd_barrier(const XcdBarrier& b) {
;     ...
;             __builtin_amdgcn_fence(__ATOMIC_ACQUIRE, "agent");
;             xb_add(&bar[XB_XGEN(b.x)], 1u);
;             asm volatile("s_waitcnt vmcnt(0)" ::: "memory");
; __global__ void __launch_bounds__(NWAVES * 64, 2) fwd(Params P) {
;     ...
;         if (IN(pb + 5)) {
;             PH_BEGIN
;             TS_BEGIN(5);
;             pg8::Gemm g{ymixb, Wout_t, D}; pg8::StaticOrder S; S.init(M, D, G, bx);
;             pg8::EpiBf16 E{(bf16_t*)mixed, FLD};
;     ...
;             { pg8::RepeatOrder R; R.init2(M, D, G, bx, 2); pg8::gemm_phase<pg8::EpiBf16, pg8::RepeatOrder>(lds, g, R, E, tid); }
;     ...
;             pg8::gemm_phase<pg8::EpiBf16, pg8::StaticOrder>(lds, g, S, E, tid);
.LBB0_1110:
	s_or_b64 exec, exec, s[6:7]
	s_waitcnt vmcnt(0)
	buffer_inv sc1
	s_waitcnt vmcnt(0)
.LBB0_1111:
	s_or_b64 exec, exec, s[2:3]
	s_mov_b32 s6, s93
	s_waitcnt lgkmcnt(0)
	s_barrier
	v_mov_b32_e32 v147, v0
	s_add_i32 s30, s6, s69
	s_cmpk_gt_i32 s30, 0x1ff
	v_readfirstlane_b32 s5, v147
	s_cbranch_scc1 .LBB0_1135
	s_ashr_i32 s31, s30, 31
	s_lshr_b32 s2, s31, 29
	s_add_i32 s8, s30, s2
	s_and_b32 s2, s8, -8
	s_sub_i32 s7, s30, s2
	s_cmp_gt_i32 s7, -1
	s_mov_b64 s[2:3], -1
	s_cbranch_scc0 .LBB0_1114
	s_lshl_b32 s4, s7, 6
	s_mov_b64 s[2:3], 0

; #define LAS __attribute__((address_space(3)))
; __device__ __forceinline__ unsigned xb_add(unsigned* p, unsigned v) { return __hip_atomic_fetch_add(p, v, __ATOMIC_RELAXED, __HIP_MEMORY_SCOPE_AGENT); }
; #define TS_BEGIN(k) do { if (TS_ON(k)) ts_t0 = __builtin_amdgcn_s_memrealtime(); } while (0)
; __device__ __forceinline__ void xcd_barrier(const XcdBarrier& b) {
;     ...
;             __builtin_amdgcn_fence(__ATOMIC_ACQUIRE, "agent");
;             xb_add(&bar[XB_XGEN(b.x)], 1u);
;             asm volatile("s_waitcnt vmcnt(0)" ::: "memory");
; __global__ void __launch_bounds__(NWAVES * 64, 2) fwd(Params P) {
;     ...
;         if (IN(pb + 6)) {
;             PH_BEGIN
;             TS_BEGIN(6);
;             const float* xin = INP(0);
;             f32x4 g8[8], b8[8];
; #pragma unroll
;             for (int j = 0; j < 8; ++j) { g8[j] = *(const f32x4*)(INP(24) + l * D + 4 * lane + 256 * j); b8[j] = *(const f32x4*)(INP(25) + l * D + 4 * lane + 256 * j); }
;             LAS float* rs = (LAS float*)lds;
;             LAS int* wgcnt = (LAS int*)(lds + 65536); LAS int* wgbase = wgcnt + 8; LAS int* rec = wgcnt + 16;
;             if (moe) { const float* router = INP(31) + (size_t)li * D * NE;
;                 for (int i = tid; i < D * NE; i += 512) rs[(i & 7) * D + (i >> 3)] = router[i];
;                 if (tid < 16) wgcnt[tid] = 0;
;                 __syncthreads(); }
.LBB0_1186:
	s_or_b64 exec, exec, s[6:7]
	s_waitcnt vmcnt(0)
	buffer_inv sc1
	s_waitcnt vmcnt(0)
.LBB0_1187:
	s_or_b64 exec, exec, s[2:3]
	s_mov_b32 s16, s93
	s_waitcnt lgkmcnt(0)
	s_barrier
	s_ashr_i32 s17, s16, 31
	s_lshl_b64 s[2:3], s[16:17], 3
	v_readlane_b32 s4, v254, 3
	v_readlane_b32 s5, v254, 4
	s_add_u32 s6, s4, s2
	v_mov_b32_e32 v132, v0
	s_addc_u32 s7, s5, s3
	s_load_dwordx4 s[8:11], s[6:7], 0xc0
	s_lshl_b32 s92, s14, 11
	s_lshl_b64 s[18:19], s[92:93], 2
	v_and_b32_e32 v74, 63, v132
	v_lshlrev_b32_e32 v68, 4, v74
	s_waitcnt lgkmcnt(0)
	s_add_u32 s2, s8, s18
	s_addc_u32 s3, s9, s19
	v_mov_b32_e32 v69, v3
	s_add_u32 s4, s10, s18
	v_lshl_add_u64 v[36:37], s[2:3], 0, v[68:69]
	s_addc_u32 s5, s11, s19
	global_load_dwordx4 v[4:7], v68, s[2:3]
	global_load_dwordx4 v[8:11], v68, s[2:3] offset:1024
	global_load_dwordx4 v[12:15], v68, s[4:5]
	global_load_dwordx4 v[16:19], v68, s[4:5] offset:1024
	global_load_dwordx4 v[20:23], v68, s[2:3] offset:2048
	global_load_dwordx4 v[24:27], v68, s[2:3] offset:3072
	global_load_dwordx4 v[28:31], v68, s[4:5] offset:2048
	global_load_dwordx4 v[32:35], v68, s[4:5] offset:3072
	s_movk_i32 s2, 0x1000
	v_add_co_u32_e32 v56, vcc, s2, v36
	v_lshl_add_u64 v[38:39], s[4:5], 0, v[68:69]
	s_nop 0
	v_addc_co_u32_e32 v57, vcc, 0, v37, vcc
	v_add_co_u32_e32 v64, vcc, 0x1000, v38
	v_readlane_b32 s2, v254, 13
	s_nop 0
	v_addc_co_u32_e32 v65, vcc, 0, v39, vcc
	global_load_dwordx4 v[36:39], v[56:57], off
	global_load_dwordx4 v[40:43], v[56:57], off offset:1024
	global_load_dwordx4 v[44:47], v[64:65], off
	global_load_dwordx4 v[48:51], v[64:65], off offset:1024
	global_load_dwordx4 v[52:55], v[56:57], off offset:2048
	s_nop 0
	global_load_dwordx4 v[56:59], v[56:57], off offset:3072
	s_nop 0
	global_load_dwordx4 v[60:63], v[64:65], off offset:2048
	s_nop 0
	global_load_dwordx4 v[64:67], v[64:65], off offset:3072
	s_load_dwordx2 s[20:21], s[6:7], 0x0
	v_readlane_b32 s3, v254, 14
	s_andn2_b64 vcc, exec, s[2:3]
	v_readfirstlane_b32 s22, v132
	v_cndmask_b32_e64 v1, 0, 1, s[2:3]
	v_cmp_ne_u32_e64 s[4:5], 1, v1
	s_cbranch_vccnz .LBB0_1204
	s_movk_i32 s2, 0x4000
	v_cmp_gt_i32_e32 vcc, s2, v132
	s_and_saveexec_b64 s[2:3], vcc
	s_cbranch_execz .LBB0_1201
	s_load_dwordx2 s[6:7], s[6:7], 0xf8
	v_max_i32_e32 v1, 0x3e00, v132
	v_sub_u32_e32 v1, v1, v132
	v_add_u32_e32 v1, 0x1ff, v1
	s_movk_i32 s8, 0x1ff
	v_cmp_lt_u32_e32 vcc, s8, v1
	s_mov_b64 s[10:11], -1
	v_mov_b32_e32 v70, v132
	s_and_saveexec_b64 s[8:9], vcc
	s_cbranch_execz .LBB0_1198
	v_readlane_b32 s10, v254, 17
	v_lshrrev_b32_e32 v1, 9, v1
	s_lshl_b32 s92, s10, 14
	s_lshl_b64 s[10:11], s[92:93], 2
	v_add_u32_e32 v69, -1, v1
	s_waitcnt lgkmcnt(0)
	s_add_u32 s10, s6, s10
	v_add_u32_e32 v133, 0x200, v132
	v_lshrrev_b32_e32 v2, 1, v69
	s_addc_u32 s11, s7, s11
	v_add_u32_e32 v2, 1, v2
	v_cmp_lt_u32_e32 vcc, 5, v69
	v_mov_b64_e32 v[70:71], v[132:133]
	s_and_saveexec_b64 s[12:13], vcc
	s_cbranch_execz .LBB0_1194
	v_and_b32_e32 v69, -4, v2
	s_mov_b64 s[14:15], 0
	v_mov_b64_e32 v[70:71], v[132:133]

; __device__ __forceinline__ float bf_lo(unsigned w) { return __uint_as_float(w << 16); }
; __device__ __forceinline__ float bf_hi(unsigned w) { return __uint_as_float(w & 0xffff0000u); }
; __device__ __forceinline__ f32x4 ld_bf4(const bf16_t* p) { const u32x2 w = *(const u32x2*)p; return (f32x4){bf_lo(w.x), bf_hi(w.x), bf_lo(w.y), bf_hi(w.y)}; }
; __global__ void __launch_bounds__(NWAVES * 64, 2) fwd(Params P) {
;     ...
;             for (int m0 = gw; m0 < M; m0 += 2 * NGW) {
;                 const int m1 = m0 + NGW; const bool has1 = m1 < M; const int m1c = has1 ? m1 : m0;
;                 f32x4 va[8], vb[8];
; #pragma unroll
;                 for (int j = 0; j < 8; ++j) { const int c = 4 * lane + 256 * j;
;                     const u32x2 ma = *(const u32x2*)((const bf16_t*)mixed + (size_t)m0 * FLD + c), mb = *(const u32x2*)((const bf16_t*)mixed + (size_t)m1c * FLD + c);
;                     const f32x4 xa = (l == 0) ? *(const f32x4*)(xin + (size_t)m0 * D + c) : ld_bf4(xb + (size_t)m0 * D + c), xbv = (l == 0) ? *(const f32x4*)(xin + (size_t)m1c * D + c) : ld_bf4(xb + (size_t)m1c * D + c);
;                     va[j] = ALPHA * xa + (f32x4){bf_lo(ma.x), bf_hi(ma.x), bf_lo(ma.y), bf_hi(ma.y)};
;                     vb[j] = ALPHA * xbv + (f32x4){bf_lo(mb.x), bf_hi(mb.x), bf_lo(mb.y), bf_hi(mb.y)}; }
.LBB0_1210:
	s_add_i32 s52, s37, s25
	s_add_i32 s51, s49, s25
	s_cmpk_lt_i32 s51, 0x4000
	s_cselect_b64 s[2:3], -1, 0
	s_and_b64 s[8:9], s[2:3], exec
	s_cselect_b32 s8, s51, s52
	v_lshl_add_u64 v[96:97], v[142:143], 0, s[16:17]
	v_mad_i64_i32 v[98:99], s[10:11], s8, v247, v[136:137]
	global_load_dwordx2 v[150:151], v[96:97], off offset:-2048
	global_load_dwordx2 v[148:149], v[98:99], off
	s_mov_b64 s[10:11], -1
	s_and_b64 vcc, exec, s[90:91]
	v_lshl_add_u64 v[146:147], v[144:145], 0, s[16:17]
	s_cbranch_vccz .LBB0_1212
	global_load_dwordx2 v[70:71], v[146:147], off offset:-2048
	s_mov_b64 s[10:11], 0
.LBB0_1212:
	s_andn2_b64 vcc, exec, s[10:11]
	s_cbranch_vccnz .LBB0_1214
	v_add_co_u32_e32 v68, vcc, 0xfffff000, v140
	s_nop 1
	v_addc_co_u32_e32 v69, vcc, -1, v141, vcc
	global_load_dwordx4 v[68:71], v[68:69], off offset:-3072
.LBB0_1214:
	s_ashr_i32 s9, s8, 31
	s_lshl_b64 s[10:11], s[8:9], 12
	s_add_u32 s12, s38, s10
	s_addc_u32 s13, s39, s11
	s_lshl_b64 s[8:9], s[8:9], 13
	s_add_u32 s10, s20, s8
	s_addc_u32 s11, s21, s9
	s_mov_b64 s[8:9], -1
	s_and_b64 vcc, exec, s[90:91]
	s_cbranch_vccz .LBB0_1216
	global_load_dwordx2 v[74:75], v134, s[12:13]
	s_mov_b64 s[8:9], 0
.LBB0_1216:
	s_andn2_b64 vcc, exec, s[8:9]
	v_lshlrev_b32_e32 v104, 2, v1
	s_cbranch_vccnz .LBB0_1218
	global_load_dwordx4 v[72:75], v104, s[10:11]
.LBB0_1218:
	global_load_dwordx2 v[154:155], v[96:97], off offset:-1536
	global_load_dwordx2 v[152:153], v[98:99], off offset:512
	v_cndmask_b32_e64 v76, 0, 1, s[90:91]
	v_cmp_ne_u32_e64 s[8:9], 1, v76
	s_andn2_b64 vcc, exec, s[90:91]
	s_mov_b64 s[14:15], -1
	s_cbranch_vccnz .LBB0_1222
	global_load_dwordx2 v[78:79], v[146:147], off offset:-1536
	s_cbranch_execz .LBB0_1223

; __device__ __forceinline__ float bf_lo(unsigned w) { return __uint_as_float(w << 16); }
; __device__ __forceinline__ float bf_hi(unsigned w) { return __uint_as_float(w & 0xffff0000u); }
; __device__ __forceinline__ f32x4 ld_bf4(const bf16_t* p) { const u32x2 w = *(const u32x2*)p; return (f32x4){bf_lo(w.x), bf_hi(w.x), bf_lo(w.y), bf_hi(w.y)}; }
; __global__ void __launch_bounds__(NWAVES * 64, 2) fwd(Params P) {
;     ...
;                 for (int j = 0; j < 8; ++j) { const int c = 4 * lane + 256 * j;
;                     const u32x2 ma = *(const u32x2*)((const bf16_t*)mixed + (size_t)m0 * FLD + c), mb = *(const u32x2*)((const bf16_t*)mixed + (size_t)m1c * FLD + c);
;                     const f32x4 xa = (l == 0) ? *(const f32x4*)(xin + (size_t)m0 * D + c) : ld_bf4(xb + (size_t)m0 * D + c), xbv = (l == 0) ? *(const f32x4*)(xin + (size_t)m1c * D + c) : ld_bf4(xb + (size_t)m1c * D + c);
;                     va[j] = ALPHA * xa + (f32x4){bf_lo(ma.x), bf_hi(ma.x), bf_lo(ma.y), bf_hi(ma.y)};
;                     vb[j] = ALPHA * xbv + (f32x4){bf_lo(mb.x), bf_hi(mb.x), bf_lo(mb.y), bf_hi(mb.y)}; }
.LBB0_1221:
	global_load_dwordx2 v[82:83], v134, s[12:13] offset:512
	s_cbranch_execz .LBB0_1225
	s_branch .LBB0_1226

; __device__ __forceinline__ float bf_lo(unsigned w) { return __uint_as_float(w << 16); }
; __device__ __forceinline__ float bf_hi(unsigned w) { return __uint_as_float(w & 0xffff0000u); }
; __device__ __forceinline__ f32x4 ld_bf4(const bf16_t* p) { const u32x2 w = *(const u32x2*)p; return (f32x4){bf_lo(w.x), bf_hi(w.x), bf_lo(w.y), bf_hi(w.y)}; }
; __global__ void __launch_bounds__(NWAVES * 64, 2) fwd(Params P) {
;     ...
;                 for (int j = 0; j < 8; ++j) { const int c = 4 * lane + 256 * j;
;                     const u32x2 ma = *(const u32x2*)((const bf16_t*)mixed + (size_t)m0 * FLD + c), mb = *(const u32x2*)((const bf16_t*)mixed + (size_t)m1c * FLD + c);
;                     const f32x4 xa = (l == 0) ? *(const f32x4*)(xin + (size_t)m0 * D + c) : ld_bf4(xb + (size_t)m0 * D + c), xbv = (l == 0) ? *(const f32x4*)(xin + (size_t)m1c * D + c) : ld_bf4(xb + (size_t)m1c * D + c);
;                     va[j] = ALPHA * xa + (f32x4){bf_lo(ma.x), bf_hi(ma.x), bf_lo(ma.y), bf_hi(ma.y)};
;                     vb[j] = ALPHA * xbv + (f32x4){bf_lo(mb.x), bf_hi(mb.x), bf_lo(mb.y), bf_hi(mb.y)}; }
.LBB0_1226:
	global_load_dwordx2 v[158:159], v[96:97], off offset:-1024
	global_load_dwordx2 v[156:157], v[98:99], off offset:1024
	s_and_b64 vcc, exec, s[8:9]
	s_mov_b64 s[14:15], -1
	s_cbranch_vccnz .LBB0_1230
	global_load_dwordx2 v[86:87], v[146:147], off offset:-1024
	s_cbranch_execz .LBB0_1231

; __device__ __forceinline__ float bf_lo(unsigned w) { return __uint_as_float(w << 16); }
; __device__ __forceinline__ float bf_hi(unsigned w) { return __uint_as_float(w & 0xffff0000u); }
; __device__ __forceinline__ f32x4 ld_bf4(const bf16_t* p) { const u32x2 w = *(const u32x2*)p; return (f32x4){bf_lo(w.x), bf_hi(w.x), bf_lo(w.y), bf_hi(w.y)}; }
; __global__ void __launch_bounds__(NWAVES * 64, 2) fwd(Params P) {
;     ...
;                 for (int j = 0; j < 8; ++j) { const int c = 4 * lane + 256 * j;
;                     const u32x2 ma = *(const u32x2*)((const bf16_t*)mixed + (size_t)m0 * FLD + c), mb = *(const u32x2*)((const bf16_t*)mixed + (size_t)m1c * FLD + c);
;                     const f32x4 xa = (l == 0) ? *(const f32x4*)(xin + (size_t)m0 * D + c) : ld_bf4(xb + (size_t)m0 * D + c), xbv = (l == 0) ? *(const f32x4*)(xin + (size_t)m1c * D + c) : ld_bf4(xb + (size_t)m1c * D + c);
;                     va[j] = ALPHA * xa + (f32x4){bf_lo(ma.x), bf_hi(ma.x), bf_lo(ma.y), bf_hi(ma.y)};
;                     vb[j] = ALPHA * xbv + (f32x4){bf_lo(mb.x), bf_hi(mb.x), bf_lo(mb.y), bf_hi(mb.y)}; }
.LBB0_1229:
	global_load_dwordx2 v[90:91], v134, s[12:13] offset:1024
	s_cbranch_execz .LBB0_1233
	s_branch .LBB0_1234

; __device__ __forceinline__ float bf_lo(unsigned w) { return __uint_as_float(w << 16); }
; __device__ __forceinline__ float bf_hi(unsigned w) { return __uint_as_float(w & 0xffff0000u); }
; __device__ __forceinline__ f32x4 ld_bf4(const bf16_t* p) { const u32x2 w = *(const u32x2*)p; return (f32x4){bf_lo(w.x), bf_hi(w.x), bf_lo(w.y), bf_hi(w.y)}; }
; __global__ void __launch_bounds__(NWAVES * 64, 2) fwd(Params P) {
;     ...
;                 for (int j = 0; j < 8; ++j) { const int c = 4 * lane + 256 * j;
;                     const u32x2 ma = *(const u32x2*)((const bf16_t*)mixed + (size_t)m0 * FLD + c), mb = *(const u32x2*)((const bf16_t*)mixed + (size_t)m1c * FLD + c);
;                     const f32x4 xa = (l == 0) ? *(const f32x4*)(xin + (size_t)m0 * D + c) : ld_bf4(xb + (size_t)m0 * D + c), xbv = (l == 0) ? *(const f32x4*)(xin + (size_t)m1c * D + c) : ld_bf4(xb + (size_t)m1c * D + c);
;                     va[j] = ALPHA * xa + (f32x4){bf_lo(ma.x), bf_hi(ma.x), bf_lo(ma.y), bf_hi(ma.y)};
;                     vb[j] = ALPHA * xbv + (f32x4){bf_lo(mb.x), bf_hi(mb.x), bf_lo(mb.y), bf_hi(mb.y)}; }
.LBB0_1234:
	global_load_dwordx2 v[172:173], v[96:97], off offset:-512
	global_load_dwordx2 v[166:167], v[98:99], off offset:1536
	s_and_b64 vcc, exec, s[8:9]
	s_mov_b64 s[14:15], -1
	s_cbranch_vccnz .LBB0_1238
	global_load_dwordx2 v[94:95], v[146:147], off offset:-512
	s_cbranch_execz .LBB0_1239

; __device__ __forceinline__ float bf_lo(unsigned w) { return __uint_as_float(w << 16); }
; __device__ __forceinline__ float bf_hi(unsigned w) { return __uint_as_float(w & 0xffff0000u); }
; __device__ __forceinline__ f32x4 ld_bf4(const bf16_t* p) { const u32x2 w = *(const u32x2*)p; return (f32x4){bf_lo(w.x), bf_hi(w.x), bf_lo(w.y), bf_hi(w.y)}; }
; __global__ void __launch_bounds__(NWAVES * 64, 2) fwd(Params P) {
;     ...
;                 for (int j = 0; j < 8; ++j) { const int c = 4 * lane + 256 * j;
;                     const u32x2 ma = *(const u32x2*)((const bf16_t*)mixed + (size_t)m0 * FLD + c), mb = *(const u32x2*)((const bf16_t*)mixed + (size_t)m1c * FLD + c);
;                     const f32x4 xa = (l == 0) ? *(const f32x4*)(xin + (size_t)m0 * D + c) : ld_bf4(xb + (size_t)m0 * D + c), xbv = (l == 0) ? *(const f32x4*)(xin + (size_t)m1c * D + c) : ld_bf4(xb + (size_t)m1c * D + c);
;                     va[j] = ALPHA * xa + (f32x4){bf_lo(ma.x), bf_hi(ma.x), bf_lo(ma.y), bf_hi(ma.y)};
;                     vb[j] = ALPHA * xbv + (f32x4){bf_lo(mb.x), bf_hi(mb.x), bf_lo(mb.y), bf_hi(mb.y)}; }
.LBB0_1237:
	global_load_dwordx2 v[102:103], v134, s[12:13] offset:1536
	s_cbranch_execz .LBB0_1241
	s_branch .LBB0_1242

; __device__ __forceinline__ float bf_lo(unsigned w) { return __uint_as_float(w << 16); }
; __device__ __forceinline__ float bf_hi(unsigned w) { return __uint_as_float(w & 0xffff0000u); }
; __device__ __forceinline__ f32x4 ld_bf4(const bf16_t* p) { const u32x2 w = *(const u32x2*)p; return (f32x4){bf_lo(w.x), bf_hi(w.x), bf_lo(w.y), bf_hi(w.y)}; }
; __global__ void __launch_bounds__(NWAVES * 64, 2) fwd(Params P) {
;     ...
;                 for (int j = 0; j < 8; ++j) { const int c = 4 * lane + 256 * j;
;                     const u32x2 ma = *(const u32x2*)((const bf16_t*)mixed + (size_t)m0 * FLD + c), mb = *(const u32x2*)((const bf16_t*)mixed + (size_t)m1c * FLD + c);
;                     const f32x4 xa = (l == 0) ? *(const f32x4*)(xin + (size_t)m0 * D + c) : ld_bf4(xb + (size_t)m0 * D + c), xbv = (l == 0) ? *(const f32x4*)(xin + (size_t)m1c * D + c) : ld_bf4(xb + (size_t)m1c * D + c);
;                     va[j] = ALPHA * xa + (f32x4){bf_lo(ma.x), bf_hi(ma.x), bf_lo(ma.y), bf_hi(ma.y)};
;                     vb[j] = ALPHA * xbv + (f32x4){bf_lo(mb.x), bf_hi(mb.x), bf_lo(mb.y), bf_hi(mb.y)}; }
.LBB0_1242:
	global_load_dwordx2 v[174:175], v[96:97], off
	global_load_dwordx2 v[178:179], v[98:99], off offset:2048
	s_and_b64 vcc, exec, s[8:9]
	s_mov_b64 s[14:15], -1
	s_cbranch_vccnz .LBB0_1246
	global_load_dwordx2 v[106:107], v[146:147], off
	s_cbranch_execz .LBB0_1247

; __device__ __forceinline__ float bf_lo(unsigned w) { return __uint_as_float(w << 16); }
; __device__ __forceinline__ float bf_hi(unsigned w) { return __uint_as_float(w & 0xffff0000u); }
; __device__ __forceinline__ f32x4 ld_bf4(const bf16_t* p) { const u32x2 w = *(const u32x2*)p; return (f32x4){bf_lo(w.x), bf_hi(w.x), bf_lo(w.y), bf_hi(w.y)}; }
; __global__ void __launch_bounds__(NWAVES * 64, 2) fwd(Params P) {
;     ...
;                 for (int j = 0; j < 8; ++j) { const int c = 4 * lane + 256 * j;
;                     const u32x2 ma = *(const u32x2*)((const bf16_t*)mixed + (size_t)m0 * FLD + c), mb = *(const u32x2*)((const bf16_t*)mixed + (size_t)m1c * FLD + c);
;                     const f32x4 xa = (l == 0) ? *(const f32x4*)(xin + (size_t)m0 * D + c) : ld_bf4(xb + (size_t)m0 * D + c), xbv = (l == 0) ? *(const f32x4*)(xin + (size_t)m1c * D + c) : ld_bf4(xb + (size_t)m1c * D + c);
;                     va[j] = ALPHA * xa + (f32x4){bf_lo(ma.x), bf_hi(ma.x), bf_lo(ma.y), bf_hi(ma.y)};
;                     vb[j] = ALPHA * xbv + (f32x4){bf_lo(mb.x), bf_hi(mb.x), bf_lo(mb.y), bf_hi(mb.y)}; }
.LBB0_1245:
	global_load_dwordx2 v[110:111], v134, s[12:13] offset:2048
	s_cbranch_execz .LBB0_1249
	s_branch .LBB0_1250

; __device__ __forceinline__ float bf_lo(unsigned w) { return __uint_as_float(w << 16); }
; __device__ __forceinline__ float bf_hi(unsigned w) { return __uint_as_float(w & 0xffff0000u); }
; __device__ __forceinline__ f32x4 ld_bf4(const bf16_t* p) { const u32x2 w = *(const u32x2*)p; return (f32x4){bf_lo(w.x), bf_hi(w.x), bf_lo(w.y), bf_hi(w.y)}; }
; __global__ void __launch_bounds__(NWAVES * 64, 2) fwd(Params P) {
;     ...
;                 for (int j = 0; j < 8; ++j) { const int c = 4 * lane + 256 * j;
;                     const u32x2 ma = *(const u32x2*)((const bf16_t*)mixed + (size_t)m0 * FLD + c), mb = *(const u32x2*)((const bf16_t*)mixed + (size_t)m1c * FLD + c);
;                     const f32x4 xa = (l == 0) ? *(const f32x4*)(xin + (size_t)m0 * D + c) : ld_bf4(xb + (size_t)m0 * D + c), xbv = (l == 0) ? *(const f32x4*)(xin + (size_t)m1c * D + c) : ld_bf4(xb + (size_t)m1c * D + c);
;                     va[j] = ALPHA * xa + (f32x4){bf_lo(ma.x), bf_hi(ma.x), bf_lo(ma.y), bf_hi(ma.y)};
;                     vb[j] = ALPHA * xbv + (f32x4){bf_lo(mb.x), bf_hi(mb.x), bf_lo(mb.y), bf_hi(mb.y)}; }
.LBB0_1250:
	global_load_dwordx2 v[168:169], v[96:97], off offset:512
	global_load_dwordx2 v[176:177], v[98:99], off offset:2560
	s_and_b64 vcc, exec, s[8:9]
	s_mov_b64 s[14:15], -1
	s_cbranch_vccnz .LBB0_1254
	global_load_dwordx2 v[118:119], v[146:147], off offset:512
	s_cbranch_execz .LBB0_1255

; __device__ __forceinline__ float bf_lo(unsigned w) { return __uint_as_float(w << 16); }
; __device__ __forceinline__ float bf_hi(unsigned w) { return __uint_as_float(w & 0xffff0000u); }
; __device__ __forceinline__ f32x4 ld_bf4(const bf16_t* p) { const u32x2 w = *(const u32x2*)p; return (f32x4){bf_lo(w.x), bf_hi(w.x), bf_lo(w.y), bf_hi(w.y)}; }
; __global__ void __launch_bounds__(NWAVES * 64, 2) fwd(Params P) {
;     ...
;                 for (int j = 0; j < 8; ++j) { const int c = 4 * lane + 256 * j;
;                     const u32x2 ma = *(const u32x2*)((const bf16_t*)mixed + (size_t)m0 * FLD + c), mb = *(const u32x2*)((const bf16_t*)mixed + (size_t)m1c * FLD + c);
;                     const f32x4 xa = (l == 0) ? *(const f32x4*)(xin + (size_t)m0 * D + c) : ld_bf4(xb + (size_t)m0 * D + c), xbv = (l == 0) ? *(const f32x4*)(xin + (size_t)m1c * D + c) : ld_bf4(xb + (size_t)m1c * D + c);
;                     va[j] = ALPHA * xa + (f32x4){bf_lo(ma.x), bf_hi(ma.x), bf_lo(ma.y), bf_hi(ma.y)};
;                     vb[j] = ALPHA * xbv + (f32x4){bf_lo(mb.x), bf_hi(mb.x), bf_lo(mb.y), bf_hi(mb.y)}; }
.LBB0_1253:
	global_load_dwordx2 v[122:123], v134, s[12:13] offset:2560
	s_cbranch_execz .LBB0_1257
	s_branch .LBB0_1258

; __device__ __forceinline__ float bf_lo(unsigned w) { return __uint_as_float(w << 16); }
; __device__ __forceinline__ float bf_hi(unsigned w) { return __uint_as_float(w & 0xffff0000u); }
; __device__ __forceinline__ f32x4 ld_bf4(const bf16_t* p) { const u32x2 w = *(const u32x2*)p; return (f32x4){bf_lo(w.x), bf_hi(w.x), bf_lo(w.y), bf_hi(w.y)}; }
; __global__ void __launch_bounds__(NWAVES * 64, 2) fwd(Params P) {
;     ...
;                 for (int j = 0; j < 8; ++j) { const int c = 4 * lane + 256 * j;
;                     const u32x2 ma = *(const u32x2*)((const bf16_t*)mixed + (size_t)m0 * FLD + c), mb = *(const u32x2*)((const bf16_t*)mixed + (size_t)m1c * FLD + c);
;                     const f32x4 xa = (l == 0) ? *(const f32x4*)(xin + (size_t)m0 * D + c) : ld_bf4(xb + (size_t)m0 * D + c), xbv = (l == 0) ? *(const f32x4*)(xin + (size_t)m1c * D + c) : ld_bf4(xb + (size_t)m1c * D + c);
;                     va[j] = ALPHA * xa + (f32x4){bf_lo(ma.x), bf_hi(ma.x), bf_lo(ma.y), bf_hi(ma.y)};
;                     vb[j] = ALPHA * xbv + (f32x4){bf_lo(mb.x), bf_hi(mb.x), bf_lo(mb.y), bf_hi(mb.y)}; }
.LBB0_1258:
	global_load_dwordx2 v[160:161], v[96:97], off offset:1024
	global_load_dwordx2 v[170:171], v[98:99], off offset:3072
	s_and_b64 vcc, exec, s[8:9]
	s_mov_b64 s[14:15], -1
	s_cbranch_vccnz .LBB0_1262
	global_load_dwordx2 v[126:127], v[146:147], off offset:1024
	s_cbranch_execz .LBB0_1263

; __device__ __forceinline__ float bf_lo(unsigned w) { return __uint_as_float(w << 16); }
; __device__ __forceinline__ float bf_hi(unsigned w) { return __uint_as_float(w & 0xffff0000u); }
; __device__ __forceinline__ f32x4 ld_bf4(const bf16_t* p) { const u32x2 w = *(const u32x2*)p; return (f32x4){bf_lo(w.x), bf_hi(w.x), bf_lo(w.y), bf_hi(w.y)}; }
; __global__ void __launch_bounds__(NWAVES * 64, 2) fwd(Params P) {
;     ...
;                 for (int j = 0; j < 8; ++j) { const int c = 4 * lane + 256 * j;
;                     const u32x2 ma = *(const u32x2*)((const bf16_t*)mixed + (size_t)m0 * FLD + c), mb = *(const u32x2*)((const bf16_t*)mixed + (size_t)m1c * FLD + c);
;                     const f32x4 xa = (l == 0) ? *(const f32x4*)(xin + (size_t)m0 * D + c) : ld_bf4(xb + (size_t)m0 * D + c), xbv = (l == 0) ? *(const f32x4*)(xin + (size_t)m1c * D + c) : ld_bf4(xb + (size_t)m1c * D + c);
;                     va[j] = ALPHA * xa + (f32x4){bf_lo(ma.x), bf_hi(ma.x), bf_lo(ma.y), bf_hi(ma.y)};
;                     vb[j] = ALPHA * xbv + (f32x4){bf_lo(mb.x), bf_hi(mb.x), bf_lo(mb.y), bf_hi(mb.y)}; }
.LBB0_1261:
	global_load_dwordx2 v[130:131], v134, s[12:13] offset:3072
	s_cbranch_execz .LBB0_1265
	s_branch .LBB0_1266

; __device__ __forceinline__ float bf_lo(unsigned w) { return __uint_as_float(w << 16); }
; __device__ __forceinline__ float bf_hi(unsigned w) { return __uint_as_float(w & 0xffff0000u); }
; __device__ __forceinline__ f32x4 ld_bf4(const bf16_t* p) { const u32x2 w = *(const u32x2*)p; return (f32x4){bf_lo(w.x), bf_hi(w.x), bf_lo(w.y), bf_hi(w.y)}; }
; __global__ void __launch_bounds__(NWAVES * 64, 2) fwd(Params P) {
;     ...
;                 for (int j = 0; j < 8; ++j) { const int c = 4 * lane + 256 * j;
;                     const u32x2 ma = *(const u32x2*)((const bf16_t*)mixed + (size_t)m0 * FLD + c), mb = *(const u32x2*)((const bf16_t*)mixed + (size_t)m1c * FLD + c);
;                     const f32x4 xa = (l == 0) ? *(const f32x4*)(xin + (size_t)m0 * D + c) : ld_bf4(xb + (size_t)m0 * D + c), xbv = (l == 0) ? *(const f32x4*)(xin + (size_t)m1c * D + c) : ld_bf4(xb + (size_t)m1c * D + c);
;                     va[j] = ALPHA * xa + (f32x4){bf_lo(ma.x), bf_hi(ma.x), bf_lo(ma.y), bf_hi(ma.y)};
;                     vb[j] = ALPHA * xbv + (f32x4){bf_lo(mb.x), bf_hi(mb.x), bf_lo(mb.y), bf_hi(mb.y)}; }
.LBB0_1266:
	global_load_dwordx2 v[180:181], v[96:97], off offset:1536
	global_load_dwordx2 v[164:165], v[98:99], off offset:3584
	s_and_b64 vcc, exec, s[8:9]
	s_mov_b64 s[14:15], -1
	s_cbranch_vccnz .LBB0_1270
	global_load_dwordx2 v[114:115], v[146:147], off offset:1536
	s_cbranch_execz .LBB0_1271

; __device__ __forceinline__ float bf_lo(unsigned w) { return __uint_as_float(w << 16); }
; __device__ __forceinline__ float bf_hi(unsigned w) { return __uint_as_float(w & 0xffff0000u); }
; __device__ __forceinline__ f32x4 ld_bf4(const bf16_t* p) { const u32x2 w = *(const u32x2*)p; return (f32x4){bf_lo(w.x), bf_hi(w.x), bf_lo(w.y), bf_hi(w.y)}; }
; __global__ void __launch_bounds__(NWAVES * 64, 2) fwd(Params P) {
;     ...
;                 for (int j = 0; j < 8; ++j) { const int c = 4 * lane + 256 * j;
;                     const u32x2 ma = *(const u32x2*)((const bf16_t*)mixed + (size_t)m0 * FLD + c), mb = *(const u32x2*)((const bf16_t*)mixed + (size_t)m1c * FLD + c);
;                     const f32x4 xa = (l == 0) ? *(const f32x4*)(xin + (size_t)m0 * D + c) : ld_bf4(xb + (size_t)m0 * D + c), xbv = (l == 0) ? *(const f32x4*)(xin + (size_t)m1c * D + c) : ld_bf4(xb + (size_t)m1c * D + c);
;                     va[j] = ALPHA * xa + (f32x4){bf_lo(ma.x), bf_hi(ma.x), bf_lo(ma.y), bf_hi(ma.y)};
;                     vb[j] = ALPHA * xbv + (f32x4){bf_lo(mb.x), bf_hi(mb.x), bf_lo(mb.y), bf_hi(mb.y)}; }
.LBB0_1269:
	global_load_dwordx2 v[98:99], v134, s[12:13] offset:3584
	s_cbranch_execz .LBB0_1273
	s_branch .LBB0_1274

; __device__ __forceinline__ float bf_lo(unsigned w) { return __uint_as_float(w << 16); }
; __device__ __forceinline__ float bf_hi(unsigned w) { return __uint_as_float(w & 0xffff0000u); }
; __device__ __forceinline__ f32x4 ld_bf4(const bf16_t* p) { const u32x2 w = *(const u32x2*)p; return (f32x4){bf_lo(w.x), bf_hi(w.x), bf_lo(w.y), bf_hi(w.y)}; }
; __global__ void __launch_bounds__(NWAVES * 64, 2) fwd(Params P) {
;     ...
;                 for (int j = 0; j < 8; ++j) { const int c = 4 * lane + 256 * j;
;                     const u32x2 ma = *(const u32x2*)((const bf16_t*)mixed + (size_t)m0 * FLD + c), mb = *(const u32x2*)((const bf16_t*)mixed + (size_t)m1c * FLD + c);
;                     const f32x4 xa = (l == 0) ? *(const f32x4*)(xin + (size_t)m0 * D + c) : ld_bf4(xb + (size_t)m0 * D + c), xbv = (l == 0) ? *(const f32x4*)(xin + (size_t)m1c * D + c) : ld_bf4(xb + (size_t)m1c * D + c);
;                     va[j] = ALPHA * xa + (f32x4){bf_lo(ma.x), bf_hi(ma.x), bf_lo(ma.y), bf_hi(ma.y)};
;                     vb[j] = ALPHA * xbv + (f32x4){bf_lo(mb.x), bf_hi(mb.x), bf_lo(mb.y), bf_hi(mb.y)}; }
.LBB0_1274:
	s_and_b64 vcc, exec, s[90:91]
	s_cbranch_vccz .Lln1_f32_path
	s_waitcnt vmcnt(0)
	v_lshlrev_b32_e32 v68, 16, v70
	v_and_b32_e32 v69, 0xffff0000, v70
	v_lshlrev_b32_e32 v70, 16, v71
	v_and_b32_e32 v71, 0xffff0000, v71
	v_lshlrev_b32_e32 v72, 16, v74
	v_and_b32_e32 v73, 0xffff0000, v74
	v_lshlrev_b32_e32 v74, 16, v75
	v_and_b32_e32 v75, 0xffff0000, v75
	v_lshlrev_b32_e32 v76, 16, v78
	v_and_b32_e32 v77, 0xffff0000, v78
	v_lshlrev_b32_e32 v78, 16, v79
	v_and_b32_e32 v79, 0xffff0000, v79
	v_lshlrev_b32_e32 v80, 16, v82
	v_and_b32_e32 v81, 0xffff0000, v82
	v_lshlrev_b32_e32 v82, 16, v83
	v_and_b32_e32 v83, 0xffff0000, v83
	v_lshlrev_b32_e32 v84, 16, v86
	v_and_b32_e32 v85, 0xffff0000, v86
	v_lshlrev_b32_e32 v86, 16, v87
	v_and_b32_e32 v87, 0xffff0000, v87
	v_lshlrev_b32_e32 v88, 16, v90
	v_and_b32_e32 v89, 0xffff0000, v90
	v_lshlrev_b32_e32 v90, 16, v91
	v_and_b32_e32 v91, 0xffff0000, v91
	v_lshlrev_b32_e32 v92, 16, v94
	v_and_b32_e32 v93, 0xffff0000, v94
	v_lshlrev_b32_e32 v94, 16, v95
	v_and_b32_e32 v95, 0xffff0000, v95
	v_lshlrev_b32_e32 v100, 16, v102
	v_and_b32_e32 v101, 0xffff0000, v102
	v_lshlrev_b32_e32 v102, 16, v103
	v_and_b32_e32 v103, 0xffff0000, v103
	v_lshlrev_b32_e32 v104, 16, v106
	v_and_b32_e32 v105, 0xffff0000, v106
	v_lshlrev_b32_e32 v106, 16, v107
	v_and_b32_e32 v107, 0xffff0000, v107
	v_lshlrev_b32_e32 v108, 16, v110
	v_and_b32_e32 v109, 0xffff0000, v110
	v_lshlrev_b32_e32 v110, 16, v111
	v_and_b32_e32 v111, 0xffff0000, v111
	v_lshlrev_b32_e32 v116, 16, v118
	v_and_b32_e32 v117, 0xffff0000, v118
	v_lshlrev_b32_e32 v118, 16, v119
	v_and_b32_e32 v119, 0xffff0000, v119
	v_lshlrev_b32_e32 v120, 16, v122
	v_and_b32_e32 v121, 0xffff0000, v122
	v_lshlrev_b32_e32 v122, 16, v123
	v_and_b32_e32 v123, 0xffff0000, v123
	v_lshlrev_b32_e32 v124, 16, v126
	v_and_b32_e32 v125, 0xffff0000, v126
	v_lshlrev_b32_e32 v126, 16, v127
	v_and_b32_e32 v127, 0xffff0000, v127
	v_lshlrev_b32_e32 v128, 16, v130
	v_and_b32_e32 v129, 0xffff0000, v130
	v_lshlrev_b32_e32 v130, 16, v131
	v_and_b32_e32 v131, 0xffff0000, v131
	v_lshlrev_b32_e32 v112, 16, v114
	v_and_b32_e32 v113, 0xffff0000, v114
	v_lshlrev_b32_e32 v114, 16, v115
	v_and_b32_e32 v115, 0xffff0000, v115
	v_lshlrev_b32_e32 v96, 16, v98
	v_and_b32_e32 v97, 0xffff0000, v98
	v_lshlrev_b32_e32 v98, 16, v99
	v_and_b32_e32 v99, 0xffff0000, v99

; template <class Epi, class Sched, bool GATHER = false>
; __device__ __forceinline__ void gemm_phase(LAS unsigned char* lds, const Gemm g, const Sched& S, const Epi& E, const int tid) {
;     const int wid = __builtin_amdgcn_readfirstlane(tid >> 6), lane = tid & 63, wr = wid >> 2, wc = wid & 3, fr = lane & 15, fq = lane >> 4;
;     const int K = g.K, nt = K / BK;
;     unsigned voffA[2], voffB[2];
; #pragma unroll
;     for (int i = 0; i < 2; ++i) { int R, C; stage_rc(tid * 16 + i * 8192, R, C); const int Rb = Epi::PERM ? ((R & ~31) + perm32(R & 31)) : R;
;         voffA[i] = (unsigned)(R * K + C) * 2u; voffB[i] = (unsigned)(Rb * K + C) * 2u; }
;     unsigned goC[2][2], goN[2][2];
;     ...
;     const size_t kstep = (size_t)(BK * 2);
;     const size_t hstep = (size_t)HALF * K * 2;
;     const size_t tstep = 2 * hstep;
;     const unsigned ldsw = (unsigned)wid * 1024u;
;     const int aoff = lds_byte(wr * 64 + fr, fq * 8), boff = lds_byte(wc * 32 + fr, fq * 8);
;     ...
;     Unit cur, nxt; int ui = 0;
;     if (!S.next(0, cur)) return;
;     f32x4 acc[2][2][4][2];
; #pragma unroll
;     for (int a = 0; a < 2; ++a)
; #pragma unroll
;         for (int b = 0; b < 2; ++b)
; #pragma unroll
;             for (int m = 0; m < 4; ++m)
; #pragma unroll
;                 for (int n = 0; n < 2; ++n) acc[a][b][m][n] = ZERO4();
;     bf16x8 At[4][2], B0[2][2], B1[2][2];
;     const char* cA = (const char*)g.A + (size_t)cur.pm * tstep; const char* cB = (const char*)g.Bt + (size_t)cur.pb * tstep;
;     ...
;     PG8_STAGE(PG8_SB(0, 0), cB, voffB); PG8_STAGE(PG8_SA(0, 0), cA, voffA); PG8_STAGE(PG8_SB(0, 1), cB + hstep, voffB); PG8_STAGE(PG8_SA(0, 1), cA + hstep, voffA);
;     if (wr == 1) PG8_BAR;
;     PG8_WAIT_V(4); PG8_BAR;
;     PG8_STAGE(PG8_SB(1, 0), cB + kstep, voffB); PG8_STAGE(PG8_SA(1, 0), cA + kstep, voffA); PG8_STAGE(PG8_SB(1, 1), cB + hstep + kstep, voffB);
;     PG8_WAIT_V(6); PG8_BAR;
;     ...
;     if (GATHER) { PG8_GLOOK(goC, cur); PG8_GLOOK(goN, cur); }
;     PG8_STAGE(PG8_SB(0, 0), cB, voffB); PG8_STAGE(PG8_SB(0, 1), cB + hstep, voffB); PG8_STAGE_A(PG8_SA(0, 0), cA, false, 0, 0); PG8_STAGE_A(PG8_SA(0, 1), cA, false, 0, 1);
;     if (wr == 1) PG8_BAR;
; __device__ __forceinline__ void xcd_barrier(const XcdBarrier& b) {
;     ...
;             __builtin_amdgcn_fence(__ATOMIC_ACQUIRE, "agent");
;             xb_add(&bar[XB_XGEN(b.x)], 1u);
;             asm volatile("s_waitcnt vmcnt(0)" ::: "memory");
.LBB0_1354:
	s_or_b64 exec, exec, s[6:7]
	s_mov_b64 s[6:7], exec
	v_mbcnt_lo_u32_b32 v1, s6, 0
	v_mbcnt_hi_u32_b32 v1, s7, v1
	v_cmp_eq_u32_e32 vcc, 0, v1
	s_and_saveexec_b64 s[8:9], vcc
	s_cbranch_execz .LBB0_1356
	s_bcnt1_i32_b64 s6, s[6:7]
	v_mov_b32_e32 v1, s6
	global_atomic_add v3, v1, s[40:41]
.LBB0_1356:
	s_or_b64 exec, exec, s[8:9]
	s_waitcnt vmcnt(0)
	buffer_inv sc1
	s_waitcnt vmcnt(0)
.LBB0_1357:
	s_or_b64 exec, exec, s[2:3]
	s_mov_b32 s46, s93
	s_waitcnt lgkmcnt(0)
	s_barrier
	s_ashr_i32 s47, s46, 31
	v_readlane_b32 s2, v253, 4
	v_readlane_b32 s3, v253, 5
	s_add_u32 s48, s2, s46
	v_readlane_b32 s2, v253, 2
	s_addc_u32 s49, s3, s47
	s_add_i32 s44, s46, s2
	s_add_i32 s45, s46, s69
	s_add_u32 s12, s48, 0xa200000
	v_readlane_b32 s2, v254, 11
	s_addc_u32 s13, s49, 0
	v_readlane_b32 s3, v254, 12
	s_add_u32 s14, s48, 0x4c000000
	v_mov_b32_e32 v134, v0
	v_cndmask_b32_e64 v1, 0, 1, s[2:3]
	s_addc_u32 s15, s49, 0
	v_cmp_ne_u32_e64 s[6:7], 1, v1
	s_andn2_b64 vcc, exec, s[2:3]
	s_mov_b64 s[2:3], -1
	s_cbranch_vccnz .LBB0_1375
	s_cmpk_gt_i32 s45, 0xaff
	v_readfirstlane_b32 s9, v134
	s_cbranch_scc1 .LBB0_1374
	v_lshlrev_b32_e32 v1, 4, v134
	s_waitcnt vmcnt(15)
	v_add_u32_e32 v4, 0x2000, v1
	v_ashrrev_i32_e32 v2, 31, v4
	v_lshrrev_b32_e32 v2, 22, v2
	v_add_u32_e32 v2, v4, v2
	v_ashrrev_i32_e32 v2, 10, v2
	v_mul_i32_i24_e32 v5, 0x400, v2
	v_sub_u32_e32 v4, v4, v5
	v_lshrrev_b32_e32 v5, 4, v4
	v_bitop3_b32 v4, v5, v4, 32 bitop3:0x6c
	v_ashrrev_i32_e32 v5, 31, v4
	v_lshrrev_b32_e32 v5, 26, v5
	v_add_u32_e32 v5, v4, v5
	v_lshlrev_b32_e32 v6, 3, v2
	v_ashrrev_i32_e32 v146, 6, v5
	v_and_b32_e32 v6, -16, v6
	v_add_u32_e32 v6, v146, v6
	v_and_b32_e32 v7, 3, v146
	s_mov_b32 s2, 0xfffe0
	s_waitcnt vmcnt(14)
	v_lshrrev_b32_e32 v8, 2, v6
	v_lshlrev_b32_e32 v9, 1, v6
	v_and_b32_e32 v5, 0xc0, v5
	v_and_or_b32 v7, v6, s2, v7
	v_and_b32_e32 v8, 4, v8
	v_and_b32_e32 v9, 24, v9
	v_sub_u32_e32 v4, v4, v5
	v_or3_b32 v7, v7, v8, v9
	v_lshlrev_b32_e32 v8, 5, v2
	v_ashrrev_i16_sdwa v4, v236, sext(v4) dst_sel:DWORD dst_unused:UNUSED_PAD src0_sel:DWORD src1_sel:BYTE_0
	v_and_b32_e32 v8, 32, v8
	v_bfe_i32 v147, v4, 0, 16
	v_add_lshl_u32 v4, v8, v147, 1
	v_lshl_add_u32 v136, v7, 12, v4
	v_lshl_add_u32 v138, v6, 12, v4
	v_bfe_i32 v4, v134, 27, 1
	v_lshrrev_b32_e32 v4, 22, v4
	v_add_u32_e32 v4, v1, v4
	v_and_b32_e32 v4, 0xfffffc00, v4
	v_sub_u32_e32 v1, v1, v4
	v_lshrrev_b32_e32 v4, 4, v1
	v_ashrrev_i32_e32 v5, 31, v134
	v_bitop3_b32 v1, v4, v1, 32 bitop3:0x6c
	v_lshrrev_b32_e32 v5, 26, v5
	v_ashrrev_i32_e32 v4, 31, v1
	v_add_u32_e32 v5, v134, v5
	v_lshrrev_b32_e32 v4, 26, v4
	v_ashrrev_i32_e32 v145, 6, v5
	v_add_u32_e32 v4, v1, v4
	v_lshlrev_b32_e32 v5, 3, v145
	v_ashrrev_i32_e32 v144, 6, v4
	v_and_b32_e32 v5, -16, v5
	v_add_u32_e32 v5, v144, v5
	v_and_b32_e32 v6, 3, v144
	s_ashr_i32 s51, s45, 31
	v_and_or_b32 v6, v5, s2, v6
	s_lshr_b32 s2, s51, 29
	s_add_i32 s2, s45, s2
	s_ashr_i32 s17, s9, 6
	s_and_b32 s3, s2, -8
	s_ashr_i32 s16, s9, 8
	s_lshl_b32 s50, s17, 10
	s_sub_i32 s3, s45, s3
	s_cmp_lt_i32 s3, 0
	s_movk_i32 s8, 0x161
	s_cselect_b32 s8, s8, 0x160
	s_mul_i32 s3, s3, s8
	s_ashr_i32 s2, s2, 3
	s_add_i32 s3, s3, s2
	s_mul_hi_i32 s2, s3, 0x2e8ba2e9
	s_lshr_b32 s8, s2, 31
	s_ashr_i32 s2, s2, 6
	s_add_i32 s2, s2, s8
	s_lshl_b32 s10, s2, 3
	s_mulk_i32 s2, 0x160
	s_sub_i32 s2, s3, s2
	s_bfe_u32 s3, s2, 0x3001c
	s_add_i32 s3, s2, s3
	s_sext_i32_i16 s8, s3
	s_and_b32 s3, s3, 0xfff8
	s_sub_i32 s2, s2, s3
	s_sext_i32_i16 s2, s2
	v_lshrrev_b32_e32 v7, 2, v5
	v_lshlrev_b32_e32 v8, 1, v5
	v_and_b32_e32 v4, 0xc0, v4
	s_lshr_b32 s8, s8, 3
	s_add_i32 s30, s10, s2
	v_and_b32_e32 v7, 4, v7
	v_and_b32_e32 v8, 24, v8
	v_sub_u32_e32 v1, v1, v4
	s_ashr_i32 s31, s30, 31
	s_bfe_i64 s[10:11], s[8:9], 0x100000
	v_or3_b32 v6, v6, v7, v8
	v_lshlrev_b32_e32 v7, 5, v145
	v_ashrrev_i16_sdwa v1, v236, sext(v1) dst_sel:DWORD dst_unused:UNUSED_PAD src0_sel:DWORD src1_sel:BYTE_0
	s_lshl_b64 s[2:3], s[30:31], 20
	s_lshl_b64 s[10:11], s[10:11], 20
	v_and_b32_e32 v7, 32, v7
	v_bfe_i32 v148, v1, 0, 16
	s_add_u32 s36, s14, s10
	v_add_lshl_u32 v1, v7, v148, 1
	s_addc_u32 s37, s15, s11
	s_add_i32 s31, s50, 0
	v_lshl_add_u32 v140, v6, 12, v1
	v_lshl_add_u32 v142, v5, 12, v1
	s_waitcnt vmcnt(10)
	v_mov_b32_e32 v25, v3
	v_mov_b32_e32 v24, v3
	v_mov_b32_e32 v23, v3
	v_mov_b32_e32 v22, v3
	v_mov_b32_e32 v21, v3
	v_mov_b32_e32 v20, v3
	v_mov_b32_e32 v19, v3
	v_mov_b32_e32 v18, v3
	s_waitcnt vmcnt(9)
	v_mov_b32_e32 v28, v3
	v_mov_b32_e32 v27, v3
	v_mov_b32_e32 v26, v3
	v_mov_b32_e32 v17, v3
	v_mov_b32_e32 v16, v3
	v_mov_b32_e32 v15, v3
	v_mov_b32_e32 v14, v3
	v_mov_b32_e32 v13, v3
	v_mov_b32_e32 v12, v3
	v_mov_b32_e32 v11, v3
	v_mov_b32_e32 v10, v3
	v_mov_b32_e32 v7, v3
	v_mov_b32_e32 v6, v3
	s_waitcnt vmcnt(1)
	v_mov_b32_e32 v63, v3
	v_mov_b32_e32 v62, v3
	v_mov_b32_e32 v89, v3
	v_mov_b32_e32 v88, v3
	v_mov_b32_e32 v87, v3
	v_mov_b32_e32 v86, v3
	v_mov_b32_e32 v85, v3
	v_mov_b32_e32 v84, v3
	v_mov_b32_e32 v83, v3
	v_mov_b32_e32 v82, v3
	v_mov_b32_e32 v1, v3
	s_add_i32 m0, s31, 0x10000
	s_nop 0
	global_load_lds_dwordx4 v140, s[36:37]
	s_add_i32 m0, s31, 0x12000
	s_add_u32 s10, s36, 0x80000
	global_load_lds_dwordx4 v136, s[36:37]
	s_addc_u32 s11, s37, 0
	s_add_i32 m0, s31, 0x14000
	v_mov_b32_e32 v141, v3
	global_load_lds_dwordx4 v140, s[10:11]
	s_add_i32 m0, s31, 0x16000
	s_add_u32 s34, s12, s2
	s_addc_u32 s35, s13, s3
	s_add_i32 s52, s31, 0x2000
	global_load_lds_dwordx4 v136, s[10:11]
	s_mov_b32 m0, s31
	s_add_u32 s2, s34, 0x80000
	global_load_lds_dwordx4 v142, s[34:35]
	s_mov_b32 m0, s52
	s_addc_u32 s3, s35, 0
	s_add_i32 s53, s31, 0x4000
	global_load_lds_dwordx4 v138, s[34:35]
	s_mov_b32 m0, s53
	s_add_i32 s54, s31, 0x6000
	global_load_lds_dwordx4 v142, s[2:3]
	s_mov_b32 m0, s54
	v_mov_b32_e32 v137, v3
	global_load_lds_dwordx4 v138, s[2:3]
	v_mov_b32_e32 v143, v3
	v_mov_b32_e32 v139, v3
	s_cmp_eq_u32 s16, 1
	v_lshl_add_u64 v[56:57], s[36:37], 0, v[140:141]
	v_lshl_add_u64 v[54:55], s[36:37], 0, v[136:137]
	v_lshl_add_u64 v[4:5], s[34:35], 0, v[142:143]
	s_cselect_b64 s[2:3], -1, 0
	s_cmp_lg_u32 s16, 1
	v_lshl_add_u64 v[8:9], s[34:35], 0, v[138:139]
	s_cbranch_scc1 .LBB0_1361
	s_barrier

; __device__ __forceinline__ unsigned xb_add(unsigned* p, unsigned v) { return __hip_atomic_fetch_add(p, v, __ATOMIC_RELAXED, __HIP_MEMORY_SCOPE_AGENT); }
; __device__ __forceinline__ void xcd_barrier(const XcdBarrier& b) {
;     ...
;             __builtin_amdgcn_fence(__ATOMIC_ACQUIRE, "agent");
;             xb_add(&bar[XB_XGEN(b.x)], 1u);
;             asm volatile("s_waitcnt vmcnt(0)" ::: "memory");
; __global__ void __launch_bounds__(NWAVES * 64, 2) fwd(Params P) {
;     ...
;             if (!moe) {
;                 pg8::Gemm g{hbuf, Wffn + (size_t)2 * DFF * D, DFF}; pg8::StaticOrder S; S.init(M, D, G, bx);
;                 pg8::EpiBf16 E{(bf16_t*)yslot, FLD};
;                 pg8::gemm_phase<pg8::EpiBf16, pg8::StaticOrder>(lds, g, S, E, tid);
.LBB0_1458:
	s_or_b64 exec, exec, s[8:9]
	s_mov_b64 s[8:9], exec
	v_mbcnt_lo_u32_b32 v1, s8, 0
	v_mbcnt_hi_u32_b32 v1, s9, v1
	v_cmp_eq_u32_e32 vcc, 0, v1
	s_and_saveexec_b64 s[10:11], vcc
	s_cbranch_execz .LBB0_1460
	s_bcnt1_i32_b64 s8, s[8:9]
	v_mov_b32_e32 v1, s8
	global_atomic_add v3, v1, s[30:31]
.LBB0_1460:
	s_or_b64 exec, exec, s[10:11]
	s_waitcnt vmcnt(0)
	buffer_inv sc1
	s_waitcnt vmcnt(0)
.LBB0_1461:
	s_or_b64 exec, exec, s[2:3]
	s_mov_b32 s22, s93
	s_waitcnt lgkmcnt(0)
	s_barrier
	s_ashr_i32 s23, s22, 31
	v_readlane_b32 s2, v253, 4
	v_readlane_b32 s3, v253, 5
	s_add_u32 s20, s2, s22
	v_readlane_b32 s2, v253, 2
	s_addc_u32 s21, s3, s23
	s_add_i32 s37, s22, s2
	s_add_i32 s36, s22, s69
	v_mov_b32_e32 v1, v0
	s_add_u32 s39, s20, 0x16400000
	s_addc_u32 s40, s21, 0
	v_readfirstlane_b32 s38, v1
	s_and_b64 vcc, exec, s[6:7]
	s_mov_b64 s[2:3], -1
	s_cbranch_vccnz .LBB0_1491
	s_cmpk_gt_i32 s36, 0x1ff
	v_readfirstlane_b32 s8, v1
	s_cbranch_scc1 .LBB0_1490
	s_ashr_i32 s41, s36, 31
	s_lshr_b32 s2, s41, 29
	s_add_i32 s11, s36, s2
	s_and_b32 s2, s11, -8
	s_sub_i32 s9, s36, s2
	s_cmp_gt_i32 s9, -1
	s_mov_b64 s[2:3], -1
	s_cbranch_scc0 .LBB0_1465
	s_lshl_b32 s12, s9, 6
	s_mov_b64 s[2:3], 0

; __device__ __forceinline__ unsigned xb_add(unsigned* p, unsigned v) { return __hip_atomic_fetch_add(p, v, __ATOMIC_RELAXED, __HIP_MEMORY_SCOPE_AGENT); }
; #define TS_BEGIN(k) do { if (TS_ON(k)) ts_t0 = __builtin_amdgcn_s_memrealtime(); } while (0)
; __device__ __forceinline__ void xcd_barrier(const XcdBarrier& b) {
;     ...
;             __builtin_amdgcn_fence(__ATOMIC_ACQUIRE, "agent");
;             xb_add(&bar[XB_XGEN(b.x)], 1u);
;             asm volatile("s_waitcnt vmcnt(0)" ::: "memory");
; __global__ void __launch_bounds__(NWAVES * 64, 2) fwd(Params P) {
;     ...
;         if (IN(pb + 10)) {
;             PH_BEGIN
;             TS_BEGIN(10);
;             f32x4 g8[8], b8[8];
; #pragma unroll
;             for (int j = 0; j < 8; ++j) { g8[j] = *(const f32x4*)(INP(26) + l * D + 4 * lane + 256 * j); b8[j] = *(const f32x4*)(INP(27) + l * D + 4 * lane + 256 * j); }
;             float* dst = (l == 3) ? P.out : (float*)nullptr; const bf16_t* ysb = (const bf16_t*)yslot;
;             int pstart[8]; { int acc_ = 0;
; #pragma unroll
;                 for (int e = 0; e < 8; ++e) { pstart[e] = acc_; acc_ += moe ? (((cnt[e] + 255) >> 8) << 8) : 0; } }
.LBB0_1780:
	s_or_b64 exec, exec, s[10:11]
	s_mov_b64 s[10:11], exec
	v_mbcnt_lo_u32_b32 v1, s10, 0
	v_mbcnt_hi_u32_b32 v1, s11, v1
	v_cmp_eq_u32_e32 vcc, 0, v1
	s_and_saveexec_b64 s[12:13], vcc
	s_cbranch_execz .LBB0_1782
	s_bcnt1_i32_b64 s10, s[10:11]
	v_mov_b32_e32 v1, s10
	v_readlane_b32 s10, v253, 17
	v_readlane_b32 s11, v253, 18
	s_nop 4
	global_atomic_add v3, v1, s[10:11]
.LBB0_1782:
	s_or_b64 exec, exec, s[12:13]
	s_waitcnt vmcnt(0)
	buffer_inv sc1
	s_waitcnt vmcnt(0)
.LBB0_1783:
	s_or_b64 exec, exec, s[8:9]
	s_mov_b32 s8, s93
	s_waitcnt lgkmcnt(0)
	s_barrier
	s_ashr_i32 s9, s8, 31
	s_lshl_b64 s[10:11], s[8:9], 3
	s_add_u32 s10, s74, s10
	v_mov_b32_e32 v68, v0
	s_addc_u32 s11, s75, s11
	s_load_dwordx4 s[12:15], s[10:11], 0xd0
	v_lshlrev_b32_e32 v1, 2, v68
	v_and_b32_e32 v69, 0xfc, v1
	v_lshlrev_b32_e32 v76, 2, v69
	v_mov_b32_e32 v77, v3
	s_waitcnt lgkmcnt(0)
	s_add_u32 s10, s12, s18
	s_addc_u32 s11, s13, s19
	s_add_u32 s12, s14, s18
	v_lshl_add_u64 v[36:37], s[10:11], 0, v[76:77]
	s_addc_u32 s13, s15, s19
	global_load_dwordx4 v[4:7], v76, s[10:11]
	global_load_dwordx4 v[8:11], v76, s[10:11] offset:1024
	global_load_dwordx4 v[12:15], v76, s[12:13]
	global_load_dwordx4 v[16:19], v76, s[12:13] offset:1024
	global_load_dwordx4 v[20:23], v76, s[10:11] offset:2048
	global_load_dwordx4 v[24:27], v76, s[10:11] offset:3072
	global_load_dwordx4 v[28:31], v76, s[12:13] offset:2048
	global_load_dwordx4 v[32:35], v76, s[12:13] offset:3072
	s_movk_i32 s10, 0x1000
	v_add_co_u32_e32 v56, vcc, s10, v36
	v_lshl_add_u64 v[38:39], s[12:13], 0, v[76:77]
	s_nop 0
	v_addc_co_u32_e32 v57, vcc, 0, v37, vcc
	v_add_co_u32_e32 v64, vcc, s10, v38
	v_readlane_b32 s10, v253, 4
	s_nop 0
	v_addc_co_u32_e32 v65, vcc, 0, v39, vcc
	global_load_dwordx4 v[36:39], v[56:57], off
	global_load_dwordx4 v[40:43], v[56:57], off offset:1024
	global_load_dwordx4 v[44:47], v[64:65], off
	global_load_dwordx4 v[48:51], v[64:65], off offset:1024
	global_load_dwordx4 v[52:55], v[56:57], off offset:2048
	s_nop 0
	global_load_dwordx4 v[56:59], v[56:57], off offset:3072
	s_nop 0
	global_load_dwordx4 v[60:63], v[64:65], off offset:2048
	s_nop 0
	global_load_dwordx4 v[64:67], v[64:65], off offset:3072
	v_readlane_b32 s11, v253, 5
	s_add_u32 s20, s10, s8
	v_readlane_b32 s10, v254, 17
	s_addc_u32 s21, s11, s9
	s_lshl_b32 s92, s10, 3
	s_lshl_b64 s[10:11], s[92:93], 2
	v_readlane_b32 s14, v254, 13
	s_add_u32 s10, s20, s10
	v_readlane_b32 s15, v254, 14
	v_readfirstlane_b32 s12, v68
	s_addc_u32 s11, s21, s11
	s_and_b64 vcc, exec, s[14:15]
	v_mov_b32_e32 v1, 0
	s_cbranch_vccz .LBB0_1785
	global_load_dword v1, v3, s[10:11] offset:64
	s_waitcnt vmcnt(0)
	v_add_u32_e32 v1, 0xff, v1
	v_and_b32_e32 v1, 0xffffff00, v1
